# baseline (speedup 1.0000x reference)
.LBB1_41:
	s_add_i32 s2, 0, 0x10200
	v_mov_b32_e32 v2, s2
	ds_read_b128 v[2:5], v2
	v_lshl_add_u32 v6, v8, 2, s4
	ds_read_b32 v56, v6 offset:256
	s_waitcnt lgkmcnt(0)
	v_lshrrev_b32_e32 v5, 5, v1
	v_lshlrev_b32_e32 v98, 4, v5
	v_add_u32_e32 v3, 0, v98
	v_add_u32_e32 v99, 0x10000, v3
	ds_read_b128 v[6:9], v99
	ds_read_b128 v[10:13], v99 offset:256
	v_mov_b32_e32 v19, s4
	ds_read_b128 v[14:17], v99 offset:32
	ds_read_b128 v[20:23], v99 offset:288
	s_add_i32 s2, 0, 0x10210
	v_mov_b32_e32 v57, s2
	s_waitcnt lgkmcnt(0)
	v_pk_fma_f32 v[44:45], v[18:19], v[6:7], v[10:11] op_sel_hi:[0,1,1]
	v_pk_fma_f32 v[46:47], v[18:19], v[8:9], v[12:13] op_sel_hi:[0,1,1]
	ds_read_b128 v[6:9], v99 offset:320
	ds_read_b128 v[10:13], v99 offset:64
	ds_read_b128 v[24:27], v99 offset:96
	ds_read_b128 v[28:31], v99 offset:352
	v_pk_fma_f32 v[40:41], v[18:19], v[14:15], v[20:21] op_sel_hi:[0,1,1]
	v_pk_fma_f32 v[42:43], v[18:19], v[16:17], v[22:23] op_sel_hi:[0,1,1]
	s_waitcnt lgkmcnt(0)
	v_pk_fma_f32 v[36:37], v[18:19], v[10:11], v[6:7] op_sel_hi:[0,1,1]
	v_pk_fma_f32 v[38:39], v[18:19], v[12:13], v[8:9] op_sel_hi:[0,1,1]
	v_pk_fma_f32 v[32:33], v[18:19], v[24:25], v[28:29] op_sel_hi:[0,1,1]
	v_pk_fma_f32 v[34:35], v[18:19], v[26:27], v[30:31] op_sel_hi:[0,1,1]
	ds_read_b128 v[6:9], v99 offset:384
	ds_read_b128 v[10:13], v99 offset:128
	ds_read_b128 v[14:17], v99 offset:160
	ds_read_b128 v[48:51], v99 offset:416
	ds_read_b128 v[20:23], v99 offset:192
	ds_read_b128 v[24:27], v99 offset:448
	s_waitcnt lgkmcnt(0)
	v_pk_fma_f32 v[28:29], v[18:19], v[10:11], v[6:7] op_sel_hi:[0,1,1]
	v_pk_fma_f32 v[30:31], v[18:19], v[12:13], v[8:9] op_sel_hi:[0,1,1]
	ds_read_b128 v[10:13], v99 offset:224
	ds_read_b128 v[52:55], v99 offset:480
	ds_read_b128 v[6:9], v57
	s_waitcnt lgkmcnt(0)
	v_lshl_add_u32 v7, v1, 2, s4
	v_fmac_f32_e32 v4, v18, v2
	v_pk_fma_f32 v[2:3], v[18:19], v[20:21], v[24:25] op_sel_hi:[0,1,1]
	v_pk_fma_f32 v[20:21], v[18:19], v[22:23], v[26:27] op_sel_hi:[0,1,1]
	ds_read_b32 v7, v7
	v_pk_fma_f32 v[22:23], v[18:19], v[10:11], v[52:53] op_sel_hi:[0,1,1]
	v_mbcnt_lo_u32_b32 v11, -1, 0
	v_mbcnt_hi_u32_b32 v52, -1, v11
	v_and_b32_e32 v11, 64, v52
	v_add_u32_e32 v53, 64, v11
	v_xor_b32_e32 v11, 1, v52
	v_cmp_lt_i32_e32 vcc, v11, v53
	v_max_f32_e32 v10, v56, v56
	s_waitcnt lgkmcnt(0)
	v_max_f32_e32 v7, v7, v7
	v_cndmask_b32_e32 v11, v52, v11, vcc
	v_max_f32_e32 v24, v7, v10
	v_lshlrev_b32_e32 v11, 2, v11
	s_add_i32 s2, 0, 0x10220
	ds_bpermute_b32 v25, v11, v24
	v_min_f32_e32 v7, v7, v10
	v_mov_b32_e32 v9, s2
	v_pk_fma_f32 v[26:27], v[18:19], v[12:13], v[54:55] op_sel_hi:[0,1,1]
	ds_bpermute_b32 v54, v11, v7
	ds_read_b128 v[10:13], v9
	s_waitcnt lgkmcnt(0)
	v_xor_b32_e32 v11, 2, v52
	v_cmp_lt_i32_e32 vcc, v11, v53
	v_fmac_f32_e32 v8, v18, v6
	v_max_f32_e32 v6, v25, v25
	v_cndmask_b32_e32 v11, v52, v11, vcc
	v_max_f32_e32 v6, v24, v6
	v_max_f32_e32 v9, v54, v54
	v_lshlrev_b32_e32 v11, 2, v11
	ds_bpermute_b32 v13, v11, v6
	v_min_f32_e32 v7, v7, v9
	ds_bpermute_b32 v9, v11, v7
	v_fmac_f32_e32 v12, v18, v10
	s_add_i32 s2, 0, 0x10230
	s_waitcnt lgkmcnt(0)
	v_max_f32_e32 v13, v13, v13
	v_max_f32_e32 v13, v6, v13
	v_max_f32_e32 v6, v9, v9
	v_xor_b32_e32 v9, 4, v52
	v_cmp_lt_i32_e32 vcc, v9, v53
	v_min_f32_e32 v55, v7, v6
	v_pk_fma_f32 v[6:7], v[18:19], v[14:15], v[48:49] op_sel_hi:[0,1,1]
	v_cndmask_b32_e32 v9, v52, v9, vcc
	v_lshlrev_b32_e32 v9, 2, v9
	ds_bpermute_b32 v54, v9, v13
	ds_bpermute_b32 v9, v9, v55
	v_mov_b32_e32 v11, s2
	s_movk_i32 s2, 0xc0
	v_pk_fma_f32 v[24:25], v[18:19], v[16:17], v[50:51] op_sel_hi:[0,1,1]
	s_waitcnt lgkmcnt(0)
	v_max_f32_e32 v14, v54, v54
	v_max_f32_e32 v13, v13, v14
	v_xor_b32_e32 v14, 8, v52
	v_cmp_lt_i32_e32 vcc, v14, v53
	v_max_f32_e32 v9, v9, v9
	v_min_f32_e32 v9, v55, v9
	v_cndmask_b32_e32 v14, v52, v14, vcc
	v_lshlrev_b32_e32 v14, 2, v14
	ds_bpermute_b32 v48, v14, v13
	ds_bpermute_b32 v49, v14, v9
	ds_read_b128 v[14:17], v11
	v_mad_u32_u24 v125, v5, s2, v19
	ds_read_b128 v[58:61], v125
	s_waitcnt lgkmcnt(0)
	v_max_f32_e32 v10, v48, v48
	v_max_f32_e32 v10, v13, v10
	v_xor_b32_e32 v13, 16, v52
	v_cmp_lt_i32_e32 vcc, v13, v53
	v_max_f32_e32 v11, v49, v49
	v_min_f32_e32 v9, v9, v11
	v_cndmask_b32_e32 v13, v52, v13, vcc
	v_lshlrev_b32_e32 v13, 2, v13
	ds_bpermute_b32 v15, v13, v10
	ds_bpermute_b32 v11, v13, v9
	v_fmac_f32_e32 v16, v18, v14
	ds_read_b128 v[86:89], v125 offset:16
	ds_read_b128 v[132:135], v125 offset:32
	s_waitcnt lgkmcnt(0)
	v_max_f32_e32 v13, v15, v15
	v_max_f32_e32 v10, v10, v13
	v_xor_b32_e32 v13, 32, v52
	v_cmp_lt_i32_e32 vcc, v13, v53
	v_max_f32_e32 v11, v11, v11
	v_min_f32_e32 v9, v9, v11
	v_cndmask_b32_e32 v13, v52, v13, vcc
	v_lshlrev_b32_e32 v13, 2, v13
	ds_bpermute_b32 v15, v13, v10
	ds_bpermute_b32 v11, v13, v9
	ds_read_b128 v[136:139], v125 offset:48
	ds_read_b128 v[148:151], v125 offset:64
	ds_read_b128 v[158:161], v125 offset:80
	ds_read_b128 v[180:183], v125 offset:96
	s_waitcnt lgkmcnt(0)
	v_max_f32_e32 v13, v15, v15
	v_max_f32_e32 v11, v11, v11
	v_max_f32_e32 v10, v10, v13
	v_min_f32_e32 v9, v9, v11
	v_mul_f32_e32 v11, v10, v4
	v_mul_f32_e32 v13, v9, v4
	v_max_f32_e32 v131, v11, v13
	v_mul_f32_e32 v11, v10, v8
	v_mul_f32_e32 v13, v9, v8
	v_max_f32_e32 v130, v11, v13
	v_mul_f32_e32 v11, v10, v12
	v_mul_f32_e32 v13, v9, v12
	v_mul_f32_e32 v10, v10, v16
	v_mul_f32_e32 v9, v9, v16
	v_max_f32_e32 v128, v10, v9
	v_max_f32_e32 v129, v11, v13
	s_waitcnt lgkmcnt(0)
	ds_read_b128 v[68:71], v125 offset:112
	ds_read_b128 v[92:95], v125 offset:128
	ds_read_b128 v[100:103], v125 offset:144
	ds_read_b128 v[104:107], v125 offset:160
	ds_read_b128 v[108:111], v125 offset:176
	v_mov_b32_e32 v140, v4
	v_mov_b32_e32 v141, v8
	v_mov_b32_e32 v142, v12
	v_mov_b32_e32 v143, v16
	v_mov_b32_e32 v144, v131
	v_mov_b32_e32 v145, v130
	v_mov_b32_e32 v146, v129
	v_mov_b32_e32 v147, v128
	v_mov_b32_e32 v152, 0
	v_mov_b32_e32 v153, 0
	v_mov_b32_e32 v154, 0
	v_mov_b32_e32 v155, 0
	v_mov_b32_e32 v164, 0
	v_mov_b32_e32 v165, 0
	v_mov_b32_e32 v166, 0
	v_mov_b32_e32 v167, 0
	v_pk_fma_f32 v[112:113], v[58:59], v[140:141], v[144:145] op_sel:[0,0,0] op_sel_hi:[0,1,1] neg_lo:[0,0,1] neg_hi:[0,0,1]
	v_pk_fma_f32 v[114:115], v[58:59], v[142:143], v[146:147] op_sel:[0,0,0] op_sel_hi:[0,1,1] neg_lo:[0,0,1] neg_hi:[0,0,1]
	v_exp_f32_e32 v112, v112
	v_exp_f32_e32 v113, v113
	v_exp_f32_e32 v114, v114
	v_exp_f32_e32 v115, v115
	v_pk_fma_f32 v[116:117], v[58:59], v[140:141], v[144:145] op_sel:[1,0,0] op_sel_hi:[1,1,1] neg_lo:[0,0,1] neg_hi:[0,0,1]
	v_pk_fma_f32 v[118:119], v[58:59], v[142:143], v[146:147] op_sel:[1,0,0] op_sel_hi:[1,1,1] neg_lo:[0,0,1] neg_hi:[0,0,1]
	v_exp_f32_e32 v116, v116
	v_exp_f32_e32 v117, v117
	v_exp_f32_e32 v118, v118
	v_exp_f32_e32 v119, v119
	v_pk_add_f32 v[152:153], v[152:153], v[112:113]
	v_pk_add_f32 v[154:155], v[154:155], v[114:115]
	v_pk_fma_f32 v[164:165], v[112:113], v[58:59], v[164:165] op_sel:[0,0,0] op_sel_hi:[1,0,1]
	v_pk_fma_f32 v[166:167], v[114:115], v[58:59], v[166:167] op_sel:[0,0,0] op_sel_hi:[1,0,1]
	v_pk_add_f32 v[152:153], v[152:153], v[116:117]
	v_pk_add_f32 v[154:155], v[154:155], v[118:119]
	v_pk_fma_f32 v[164:165], v[116:117], v[58:59], v[164:165] op_sel:[0,1,0] op_sel_hi:[1,1,1]
	v_pk_fma_f32 v[166:167], v[118:119], v[58:59], v[166:167] op_sel:[0,1,0] op_sel_hi:[1,1,1]
	v_pk_fma_f32 v[112:113], v[60:61], v[140:141], v[144:145] op_sel:[0,0,0] op_sel_hi:[0,1,1] neg_lo:[0,0,1] neg_hi:[0,0,1]
	v_pk_fma_f32 v[114:115], v[60:61], v[142:143], v[146:147] op_sel:[0,0,0] op_sel_hi:[0,1,1] neg_lo:[0,0,1] neg_hi:[0,0,1]
	v_exp_f32_e32 v112, v112
	v_exp_f32_e32 v113, v113
	v_exp_f32_e32 v114, v114
	v_exp_f32_e32 v115, v115
	v_pk_fma_f32 v[116:117], v[60:61], v[140:141], v[144:145] op_sel:[1,0,0] op_sel_hi:[1,1,1] neg_lo:[0,0,1] neg_hi:[0,0,1]
	v_pk_fma_f32 v[118:119], v[60:61], v[142:143], v[146:147] op_sel:[1,0,0] op_sel_hi:[1,1,1] neg_lo:[0,0,1] neg_hi:[0,0,1]
	v_exp_f32_e32 v116, v116
	v_exp_f32_e32 v117, v117
	v_exp_f32_e32 v118, v118
	v_exp_f32_e32 v119, v119
	v_pk_add_f32 v[152:153], v[152:153], v[112:113]
	v_pk_add_f32 v[154:155], v[154:155], v[114:115]
	v_pk_fma_f32 v[164:165], v[112:113], v[60:61], v[164:165] op_sel:[0,0,0] op_sel_hi:[1,0,1]
	v_pk_fma_f32 v[166:167], v[114:115], v[60:61], v[166:167] op_sel:[0,0,0] op_sel_hi:[1,0,1]
	v_pk_add_f32 v[152:153], v[152:153], v[116:117]
	v_pk_add_f32 v[154:155], v[154:155], v[118:119]
	v_pk_fma_f32 v[164:165], v[116:117], v[60:61], v[164:165] op_sel:[0,1,0] op_sel_hi:[1,1,1]
	v_pk_fma_f32 v[166:167], v[118:119], v[60:61], v[166:167] op_sel:[0,1,0] op_sel_hi:[1,1,1]
	v_pk_fma_f32 v[112:113], v[86:87], v[140:141], v[144:145] op_sel:[0,0,0] op_sel_hi:[0,1,1] neg_lo:[0,0,1] neg_hi:[0,0,1]
	v_pk_fma_f32 v[114:115], v[86:87], v[142:143], v[146:147] op_sel:[0,0,0] op_sel_hi:[0,1,1] neg_lo:[0,0,1] neg_hi:[0,0,1]
	v_exp_f32_e32 v112, v112
	v_exp_f32_e32 v113, v113
	v_exp_f32_e32 v114, v114
	v_exp_f32_e32 v115, v115
	v_pk_fma_f32 v[116:117], v[86:87], v[140:141], v[144:145] op_sel:[1,0,0] op_sel_hi:[1,1,1] neg_lo:[0,0,1] neg_hi:[0,0,1]
	v_pk_fma_f32 v[118:119], v[86:87], v[142:143], v[146:147] op_sel:[1,0,0] op_sel_hi:[1,1,1] neg_lo:[0,0,1] neg_hi:[0,0,1]
	v_exp_f32_e32 v116, v116
	v_exp_f32_e32 v117, v117
	v_exp_f32_e32 v118, v118
	v_exp_f32_e32 v119, v119
	v_pk_add_f32 v[152:153], v[152:153], v[112:113]
	v_pk_add_f32 v[154:155], v[154:155], v[114:115]
	v_pk_fma_f32 v[164:165], v[112:113], v[86:87], v[164:165] op_sel:[0,0,0] op_sel_hi:[1,0,1]
	v_pk_fma_f32 v[166:167], v[114:115], v[86:87], v[166:167] op_sel:[0,0,0] op_sel_hi:[1,0,1]
	v_pk_add_f32 v[152:153], v[152:153], v[116:117]
	v_pk_add_f32 v[154:155], v[154:155], v[118:119]
	v_pk_fma_f32 v[164:165], v[116:117], v[86:87], v[164:165] op_sel:[0,1,0] op_sel_hi:[1,1,1]
	v_pk_fma_f32 v[166:167], v[118:119], v[86:87], v[166:167] op_sel:[0,1,0] op_sel_hi:[1,1,1]
	v_pk_fma_f32 v[112:113], v[88:89], v[140:141], v[144:145] op_sel:[0,0,0] op_sel_hi:[0,1,1] neg_lo:[0,0,1] neg_hi:[0,0,1]
	v_pk_fma_f32 v[114:115], v[88:89], v[142:143], v[146:147] op_sel:[0,0,0] op_sel_hi:[0,1,1] neg_lo:[0,0,1] neg_hi:[0,0,1]
	v_exp_f32_e32 v112, v112
	v_exp_f32_e32 v113, v113
	v_exp_f32_e32 v114, v114
	v_exp_f32_e32 v115, v115
	v_pk_fma_f32 v[116:117], v[88:89], v[140:141], v[144:145] op_sel:[1,0,0] op_sel_hi:[1,1,1] neg_lo:[0,0,1] neg_hi:[0,0,1]
	v_pk_fma_f32 v[118:119], v[88:89], v[142:143], v[146:147] op_sel:[1,0,0] op_sel_hi:[1,1,1] neg_lo:[0,0,1] neg_hi:[0,0,1]
	v_exp_f32_e32 v116, v116
	v_exp_f32_e32 v117, v117
	v_exp_f32_e32 v118, v118
	v_exp_f32_e32 v119, v119
	v_pk_add_f32 v[152:153], v[152:153], v[112:113]
	v_pk_add_f32 v[154:155], v[154:155], v[114:115]
	v_pk_fma_f32 v[164:165], v[112:113], v[88:89], v[164:165] op_sel:[0,0,0] op_sel_hi:[1,0,1]
	v_pk_fma_f32 v[166:167], v[114:115], v[88:89], v[166:167] op_sel:[0,0,0] op_sel_hi:[1,0,1]
	v_pk_add_f32 v[152:153], v[152:153], v[116:117]
	v_pk_add_f32 v[154:155], v[154:155], v[118:119]
	v_pk_fma_f32 v[164:165], v[116:117], v[88:89], v[164:165] op_sel:[0,1,0] op_sel_hi:[1,1,1]
	v_pk_fma_f32 v[166:167], v[118:119], v[88:89], v[166:167] op_sel:[0,1,0] op_sel_hi:[1,1,1]
	v_pk_fma_f32 v[112:113], v[132:133], v[140:141], v[144:145] op_sel:[0,0,0] op_sel_hi:[0,1,1] neg_lo:[0,0,1] neg_hi:[0,0,1]
	v_pk_fma_f32 v[114:115], v[132:133], v[142:143], v[146:147] op_sel:[0,0,0] op_sel_hi:[0,1,1] neg_lo:[0,0,1] neg_hi:[0,0,1]
	v_exp_f32_e32 v112, v112
	v_exp_f32_e32 v113, v113
	v_exp_f32_e32 v114, v114
	v_exp_f32_e32 v115, v115
	v_pk_fma_f32 v[116:117], v[132:133], v[140:141], v[144:145] op_sel:[1,0,0] op_sel_hi:[1,1,1] neg_lo:[0,0,1] neg_hi:[0,0,1]
	v_pk_fma_f32 v[118:119], v[132:133], v[142:143], v[146:147] op_sel:[1,0,0] op_sel_hi:[1,1,1] neg_lo:[0,0,1] neg_hi:[0,0,1]
	v_exp_f32_e32 v116, v116
	v_exp_f32_e32 v117, v117
	v_exp_f32_e32 v118, v118
	v_exp_f32_e32 v119, v119
	v_pk_add_f32 v[152:153], v[152:153], v[112:113]
	v_pk_add_f32 v[154:155], v[154:155], v[114:115]
	v_pk_fma_f32 v[164:165], v[112:113], v[132:133], v[164:165] op_sel:[0,0,0] op_sel_hi:[1,0,1]
	v_pk_fma_f32 v[166:167], v[114:115], v[132:133], v[166:167] op_sel:[0,0,0] op_sel_hi:[1,0,1]
	v_pk_add_f32 v[152:153], v[152:153], v[116:117]
	v_pk_add_f32 v[154:155], v[154:155], v[118:119]
	v_pk_fma_f32 v[164:165], v[116:117], v[132:133], v[164:165] op_sel:[0,1,0] op_sel_hi:[1,1,1]
	v_pk_fma_f32 v[166:167], v[118:119], v[132:133], v[166:167] op_sel:[0,1,0] op_sel_hi:[1,1,1]
	v_pk_fma_f32 v[112:113], v[134:135], v[140:141], v[144:145] op_sel:[0,0,0] op_sel_hi:[0,1,1] neg_lo:[0,0,1] neg_hi:[0,0,1]
	v_pk_fma_f32 v[114:115], v[134:135], v[142:143], v[146:147] op_sel:[0,0,0] op_sel_hi:[0,1,1] neg_lo:[0,0,1] neg_hi:[0,0,1]
	v_exp_f32_e32 v112, v112
	v_exp_f32_e32 v113, v113
	v_exp_f32_e32 v114, v114
	v_exp_f32_e32 v115, v115
	v_pk_fma_f32 v[116:117], v[134:135], v[140:141], v[144:145] op_sel:[1,0,0] op_sel_hi:[1,1,1] neg_lo:[0,0,1] neg_hi:[0,0,1]
	v_pk_fma_f32 v[118:119], v[134:135], v[142:143], v[146:147] op_sel:[1,0,0] op_sel_hi:[1,1,1] neg_lo:[0,0,1] neg_hi:[0,0,1]
	v_exp_f32_e32 v116, v116
	v_exp_f32_e32 v117, v117
	v_exp_f32_e32 v118, v118
	v_exp_f32_e32 v119, v119
	v_pk_add_f32 v[152:153], v[152:153], v[112:113]
	v_pk_add_f32 v[154:155], v[154:155], v[114:115]
	v_pk_fma_f32 v[164:165], v[112:113], v[134:135], v[164:165] op_sel:[0,0,0] op_sel_hi:[1,0,1]
	v_pk_fma_f32 v[166:167], v[114:115], v[134:135], v[166:167] op_sel:[0,0,0] op_sel_hi:[1,0,1]
	v_pk_add_f32 v[152:153], v[152:153], v[116:117]
	v_pk_add_f32 v[154:155], v[154:155], v[118:119]
	v_pk_fma_f32 v[164:165], v[116:117], v[134:135], v[164:165] op_sel:[0,1,0] op_sel_hi:[1,1,1]
	v_pk_fma_f32 v[166:167], v[118:119], v[134:135], v[166:167] op_sel:[0,1,0] op_sel_hi:[1,1,1]
	v_pk_fma_f32 v[112:113], v[136:137], v[140:141], v[144:145] op_sel:[0,0,0] op_sel_hi:[0,1,1] neg_lo:[0,0,1] neg_hi:[0,0,1]
	v_pk_fma_f32 v[114:115], v[136:137], v[142:143], v[146:147] op_sel:[0,0,0] op_sel_hi:[0,1,1] neg_lo:[0,0,1] neg_hi:[0,0,1]
	v_exp_f32_e32 v112, v112
	v_exp_f32_e32 v113, v113
	v_exp_f32_e32 v114, v114
	v_exp_f32_e32 v115, v115
	v_pk_fma_f32 v[116:117], v[136:137], v[140:141], v[144:145] op_sel:[1,0,0] op_sel_hi:[1,1,1] neg_lo:[0,0,1] neg_hi:[0,0,1]
	v_pk_fma_f32 v[118:119], v[136:137], v[142:143], v[146:147] op_sel:[1,0,0] op_sel_hi:[1,1,1] neg_lo:[0,0,1] neg_hi:[0,0,1]
	v_exp_f32_e32 v116, v116
	v_exp_f32_e32 v117, v117
	v_exp_f32_e32 v118, v118
	v_exp_f32_e32 v119, v119
	v_pk_add_f32 v[152:153], v[152:153], v[112:113]
	v_pk_add_f32 v[154:155], v[154:155], v[114:115]
	v_pk_fma_f32 v[164:165], v[112:113], v[136:137], v[164:165] op_sel:[0,0,0] op_sel_hi:[1,0,1]
	v_pk_fma_f32 v[166:167], v[114:115], v[136:137], v[166:167] op_sel:[0,0,0] op_sel_hi:[1,0,1]
	v_pk_add_f32 v[152:153], v[152:153], v[116:117]
	v_pk_add_f32 v[154:155], v[154:155], v[118:119]
	v_pk_fma_f32 v[164:165], v[116:117], v[136:137], v[164:165] op_sel:[0,1,0] op_sel_hi:[1,1,1]
	v_pk_fma_f32 v[166:167], v[118:119], v[136:137], v[166:167] op_sel:[0,1,0] op_sel_hi:[1,1,1]
	v_pk_fma_f32 v[112:113], v[138:139], v[140:141], v[144:145] op_sel:[0,0,0] op_sel_hi:[0,1,1] neg_lo:[0,0,1] neg_hi:[0,0,1]
	v_pk_fma_f32 v[114:115], v[138:139], v[142:143], v[146:147] op_sel:[0,0,0] op_sel_hi:[0,1,1] neg_lo:[0,0,1] neg_hi:[0,0,1]
	v_exp_f32_e32 v112, v112
	v_exp_f32_e32 v113, v113
	v_exp_f32_e32 v114, v114
	v_exp_f32_e32 v115, v115
	v_pk_fma_f32 v[116:117], v[138:139], v[140:141], v[144:145] op_sel:[1,0,0] op_sel_hi:[1,1,1] neg_lo:[0,0,1] neg_hi:[0,0,1]
	v_pk_fma_f32 v[118:119], v[138:139], v[142:143], v[146:147] op_sel:[1,0,0] op_sel_hi:[1,1,1] neg_lo:[0,0,1] neg_hi:[0,0,1]
	v_exp_f32_e32 v116, v116
	v_exp_f32_e32 v117, v117
	v_exp_f32_e32 v118, v118
	v_exp_f32_e32 v119, v119
	v_pk_add_f32 v[152:153], v[152:153], v[112:113]
	v_pk_add_f32 v[154:155], v[154:155], v[114:115]
	v_pk_fma_f32 v[164:165], v[112:113], v[138:139], v[164:165] op_sel:[0,0,0] op_sel_hi:[1,0,1]
	v_pk_fma_f32 v[166:167], v[114:115], v[138:139], v[166:167] op_sel:[0,0,0] op_sel_hi:[1,0,1]
	v_pk_add_f32 v[152:153], v[152:153], v[116:117]
	v_pk_add_f32 v[154:155], v[154:155], v[118:119]
	v_pk_fma_f32 v[164:165], v[116:117], v[138:139], v[164:165] op_sel:[0,1,0] op_sel_hi:[1,1,1]
	v_pk_fma_f32 v[166:167], v[118:119], v[138:139], v[166:167] op_sel:[0,1,0] op_sel_hi:[1,1,1]
	v_pk_fma_f32 v[112:113], v[148:149], v[140:141], v[144:145] op_sel:[0,0,0] op_sel_hi:[0,1,1] neg_lo:[0,0,1] neg_hi:[0,0,1]
	v_pk_fma_f32 v[114:115], v[148:149], v[142:143], v[146:147] op_sel:[0,0,0] op_sel_hi:[0,1,1] neg_lo:[0,0,1] neg_hi:[0,0,1]
	v_exp_f32_e32 v112, v112
	v_exp_f32_e32 v113, v113
	v_exp_f32_e32 v114, v114
	v_exp_f32_e32 v115, v115
	v_pk_fma_f32 v[116:117], v[148:149], v[140:141], v[144:145] op_sel:[1,0,0] op_sel_hi:[1,1,1] neg_lo:[0,0,1] neg_hi:[0,0,1]
	v_pk_fma_f32 v[118:119], v[148:149], v[142:143], v[146:147] op_sel:[1,0,0] op_sel_hi:[1,1,1] neg_lo:[0,0,1] neg_hi:[0,0,1]
	v_exp_f32_e32 v116, v116
	v_exp_f32_e32 v117, v117
	v_exp_f32_e32 v118, v118
	v_exp_f32_e32 v119, v119
	v_pk_add_f32 v[152:153], v[152:153], v[112:113]
	v_pk_add_f32 v[154:155], v[154:155], v[114:115]
	v_pk_fma_f32 v[164:165], v[112:113], v[148:149], v[164:165] op_sel:[0,0,0] op_sel_hi:[1,0,1]
	v_pk_fma_f32 v[166:167], v[114:115], v[148:149], v[166:167] op_sel:[0,0,0] op_sel_hi:[1,0,1]
	v_pk_add_f32 v[152:153], v[152:153], v[116:117]
	v_pk_add_f32 v[154:155], v[154:155], v[118:119]
	v_pk_fma_f32 v[164:165], v[116:117], v[148:149], v[164:165] op_sel:[0,1,0] op_sel_hi:[1,1,1]
	v_pk_fma_f32 v[166:167], v[118:119], v[148:149], v[166:167] op_sel:[0,1,0] op_sel_hi:[1,1,1]
	v_pk_fma_f32 v[112:113], v[150:151], v[140:141], v[144:145] op_sel:[0,0,0] op_sel_hi:[0,1,1] neg_lo:[0,0,1] neg_hi:[0,0,1]
	v_pk_fma_f32 v[114:115], v[150:151], v[142:143], v[146:147] op_sel:[0,0,0] op_sel_hi:[0,1,1] neg_lo:[0,0,1] neg_hi:[0,0,1]
	v_exp_f32_e32 v112, v112
	v_exp_f32_e32 v113, v113
	v_exp_f32_e32 v114, v114
	v_exp_f32_e32 v115, v115
	v_pk_fma_f32 v[116:117], v[150:151], v[140:141], v[144:145] op_sel:[1,0,0] op_sel_hi:[1,1,1] neg_lo:[0,0,1] neg_hi:[0,0,1]
	v_pk_fma_f32 v[118:119], v[150:151], v[142:143], v[146:147] op_sel:[1,0,0] op_sel_hi:[1,1,1] neg_lo:[0,0,1] neg_hi:[0,0,1]
	v_exp_f32_e32 v116, v116
	v_exp_f32_e32 v117, v117
	v_exp_f32_e32 v118, v118
	v_exp_f32_e32 v119, v119
	v_pk_add_f32 v[152:153], v[152:153], v[112:113]
	v_pk_add_f32 v[154:155], v[154:155], v[114:115]
	v_pk_fma_f32 v[164:165], v[112:113], v[150:151], v[164:165] op_sel:[0,0,0] op_sel_hi:[1,0,1]
	v_pk_fma_f32 v[166:167], v[114:115], v[150:151], v[166:167] op_sel:[0,0,0] op_sel_hi:[1,0,1]
	v_pk_add_f32 v[152:153], v[152:153], v[116:117]
	v_pk_add_f32 v[154:155], v[154:155], v[118:119]
	v_pk_fma_f32 v[164:165], v[116:117], v[150:151], v[164:165] op_sel:[0,1,0] op_sel_hi:[1,1,1]
	v_pk_fma_f32 v[166:167], v[118:119], v[150:151], v[166:167] op_sel:[0,1,0] op_sel_hi:[1,1,1]
	v_pk_fma_f32 v[112:113], v[158:159], v[140:141], v[144:145] op_sel:[0,0,0] op_sel_hi:[0,1,1] neg_lo:[0,0,1] neg_hi:[0,0,1]
	v_pk_fma_f32 v[114:115], v[158:159], v[142:143], v[146:147] op_sel:[0,0,0] op_sel_hi:[0,1,1] neg_lo:[0,0,1] neg_hi:[0,0,1]
	v_exp_f32_e32 v112, v112
	v_exp_f32_e32 v113, v113
	v_exp_f32_e32 v114, v114
	v_exp_f32_e32 v115, v115
	v_pk_fma_f32 v[116:117], v[158:159], v[140:141], v[144:145] op_sel:[1,0,0] op_sel_hi:[1,1,1] neg_lo:[0,0,1] neg_hi:[0,0,1]
	v_pk_fma_f32 v[118:119], v[158:159], v[142:143], v[146:147] op_sel:[1,0,0] op_sel_hi:[1,1,1] neg_lo:[0,0,1] neg_hi:[0,0,1]
	v_exp_f32_e32 v116, v116
	v_exp_f32_e32 v117, v117
	v_exp_f32_e32 v118, v118
	v_exp_f32_e32 v119, v119
	v_pk_add_f32 v[152:153], v[152:153], v[112:113]
	v_pk_add_f32 v[154:155], v[154:155], v[114:115]
	v_pk_fma_f32 v[164:165], v[112:113], v[158:159], v[164:165] op_sel:[0,0,0] op_sel_hi:[1,0,1]
	v_pk_fma_f32 v[166:167], v[114:115], v[158:159], v[166:167] op_sel:[0,0,0] op_sel_hi:[1,0,1]
	v_pk_add_f32 v[152:153], v[152:153], v[116:117]
	v_pk_add_f32 v[154:155], v[154:155], v[118:119]
	v_pk_fma_f32 v[164:165], v[116:117], v[158:159], v[164:165] op_sel:[0,1,0] op_sel_hi:[1,1,1]
	v_pk_fma_f32 v[166:167], v[118:119], v[158:159], v[166:167] op_sel:[0,1,0] op_sel_hi:[1,1,1]
	v_pk_fma_f32 v[112:113], v[160:161], v[140:141], v[144:145] op_sel:[0,0,0] op_sel_hi:[0,1,1] neg_lo:[0,0,1] neg_hi:[0,0,1]
	v_pk_fma_f32 v[114:115], v[160:161], v[142:143], v[146:147] op_sel:[0,0,0] op_sel_hi:[0,1,1] neg_lo:[0,0,1] neg_hi:[0,0,1]
	v_exp_f32_e32 v112, v112
	v_exp_f32_e32 v113, v113
	v_exp_f32_e32 v114, v114
	v_exp_f32_e32 v115, v115
	v_pk_fma_f32 v[116:117], v[160:161], v[140:141], v[144:145] op_sel:[1,0,0] op_sel_hi:[1,1,1] neg_lo:[0,0,1] neg_hi:[0,0,1]
	v_pk_fma_f32 v[118:119], v[160:161], v[142:143], v[146:147] op_sel:[1,0,0] op_sel_hi:[1,1,1] neg_lo:[0,0,1] neg_hi:[0,0,1]
	v_exp_f32_e32 v116, v116
	v_exp_f32_e32 v117, v117
	v_exp_f32_e32 v118, v118
	v_exp_f32_e32 v119, v119
	v_pk_add_f32 v[152:153], v[152:153], v[112:113]
	v_pk_add_f32 v[154:155], v[154:155], v[114:115]
	v_pk_fma_f32 v[164:165], v[112:113], v[160:161], v[164:165] op_sel:[0,0,0] op_sel_hi:[1,0,1]
	v_pk_fma_f32 v[166:167], v[114:115], v[160:161], v[166:167] op_sel:[0,0,0] op_sel_hi:[1,0,1]
	v_pk_add_f32 v[152:153], v[152:153], v[116:117]
	v_pk_add_f32 v[154:155], v[154:155], v[118:119]
	v_pk_fma_f32 v[164:165], v[116:117], v[160:161], v[164:165] op_sel:[0,1,0] op_sel_hi:[1,1,1]
	v_pk_fma_f32 v[166:167], v[118:119], v[160:161], v[166:167] op_sel:[0,1,0] op_sel_hi:[1,1,1]
	v_pk_fma_f32 v[112:113], v[180:181], v[140:141], v[144:145] op_sel:[0,0,0] op_sel_hi:[0,1,1] neg_lo:[0,0,1] neg_hi:[0,0,1]
	v_pk_fma_f32 v[114:115], v[180:181], v[142:143], v[146:147] op_sel:[0,0,0] op_sel_hi:[0,1,1] neg_lo:[0,0,1] neg_hi:[0,0,1]
	v_exp_f32_e32 v112, v112
	v_exp_f32_e32 v113, v113
	v_exp_f32_e32 v114, v114
	v_exp_f32_e32 v115, v115
	v_pk_fma_f32 v[116:117], v[180:181], v[140:141], v[144:145] op_sel:[1,0,0] op_sel_hi:[1,1,1] neg_lo:[0,0,1] neg_hi:[0,0,1]
	v_pk_fma_f32 v[118:119], v[180:181], v[142:143], v[146:147] op_sel:[1,0,0] op_sel_hi:[1,1,1] neg_lo:[0,0,1] neg_hi:[0,0,1]
	v_exp_f32_e32 v116, v116
	v_exp_f32_e32 v117, v117
	v_exp_f32_e32 v118, v118
	v_exp_f32_e32 v119, v119
	v_pk_add_f32 v[152:153], v[152:153], v[112:113]
	v_pk_add_f32 v[154:155], v[154:155], v[114:115]
	v_pk_fma_f32 v[164:165], v[112:113], v[180:181], v[164:165] op_sel:[0,0,0] op_sel_hi:[1,0,1]
	v_pk_fma_f32 v[166:167], v[114:115], v[180:181], v[166:167] op_sel:[0,0,0] op_sel_hi:[1,0,1]
	v_pk_add_f32 v[152:153], v[152:153], v[116:117]
	v_pk_add_f32 v[154:155], v[154:155], v[118:119]
	v_pk_fma_f32 v[164:165], v[116:117], v[180:181], v[164:165] op_sel:[0,1,0] op_sel_hi:[1,1,1]
	v_pk_fma_f32 v[166:167], v[118:119], v[180:181], v[166:167] op_sel:[0,1,0] op_sel_hi:[1,1,1]
	v_pk_fma_f32 v[112:113], v[182:183], v[140:141], v[144:145] op_sel:[0,0,0] op_sel_hi:[0,1,1] neg_lo:[0,0,1] neg_hi:[0,0,1]
	v_pk_fma_f32 v[114:115], v[182:183], v[142:143], v[146:147] op_sel:[0,0,0] op_sel_hi:[0,1,1] neg_lo:[0,0,1] neg_hi:[0,0,1]
	v_exp_f32_e32 v112, v112
	v_exp_f32_e32 v113, v113
	v_exp_f32_e32 v114, v114
	v_exp_f32_e32 v115, v115
	v_pk_fma_f32 v[116:117], v[182:183], v[140:141], v[144:145] op_sel:[1,0,0] op_sel_hi:[1,1,1] neg_lo:[0,0,1] neg_hi:[0,0,1]
	v_pk_fma_f32 v[118:119], v[182:183], v[142:143], v[146:147] op_sel:[1,0,0] op_sel_hi:[1,1,1] neg_lo:[0,0,1] neg_hi:[0,0,1]
	v_exp_f32_e32 v116, v116
	v_exp_f32_e32 v117, v117
	v_exp_f32_e32 v118, v118
	v_exp_f32_e32 v119, v119
	v_pk_add_f32 v[152:153], v[152:153], v[112:113]
	v_pk_add_f32 v[154:155], v[154:155], v[114:115]
	v_pk_fma_f32 v[164:165], v[112:113], v[182:183], v[164:165] op_sel:[0,0,0] op_sel_hi:[1,0,1]
	v_pk_fma_f32 v[166:167], v[114:115], v[182:183], v[166:167] op_sel:[0,0,0] op_sel_hi:[1,0,1]
	v_pk_add_f32 v[152:153], v[152:153], v[116:117]
	v_pk_add_f32 v[154:155], v[154:155], v[118:119]
	v_pk_fma_f32 v[164:165], v[116:117], v[182:183], v[164:165] op_sel:[0,1,0] op_sel_hi:[1,1,1]
	v_pk_fma_f32 v[166:167], v[118:119], v[182:183], v[166:167] op_sel:[0,1,0] op_sel_hi:[1,1,1]
	s_waitcnt lgkmcnt(0)
	v_pk_fma_f32 v[112:113], v[68:69], v[140:141], v[144:145] op_sel:[0,0,0] op_sel_hi:[0,1,1] neg_lo:[0,0,1] neg_hi:[0,0,1]
	v_pk_fma_f32 v[114:115], v[68:69], v[142:143], v[146:147] op_sel:[0,0,0] op_sel_hi:[0,1,1] neg_lo:[0,0,1] neg_hi:[0,0,1]
	v_exp_f32_e32 v112, v112
	v_exp_f32_e32 v113, v113
	v_exp_f32_e32 v114, v114
	v_exp_f32_e32 v115, v115
	v_pk_fma_f32 v[116:117], v[68:69], v[140:141], v[144:145] op_sel:[1,0,0] op_sel_hi:[1,1,1] neg_lo:[0,0,1] neg_hi:[0,0,1]
	v_pk_fma_f32 v[118:119], v[68:69], v[142:143], v[146:147] op_sel:[1,0,0] op_sel_hi:[1,1,1] neg_lo:[0,0,1] neg_hi:[0,0,1]
	v_exp_f32_e32 v116, v116
	v_exp_f32_e32 v117, v117
	v_exp_f32_e32 v118, v118
	v_exp_f32_e32 v119, v119
	v_pk_add_f32 v[152:153], v[152:153], v[112:113]
	v_pk_add_f32 v[154:155], v[154:155], v[114:115]
	v_pk_fma_f32 v[164:165], v[112:113], v[68:69], v[164:165] op_sel:[0,0,0] op_sel_hi:[1,0,1]
	v_pk_fma_f32 v[166:167], v[114:115], v[68:69], v[166:167] op_sel:[0,0,0] op_sel_hi:[1,0,1]
	v_pk_add_f32 v[152:153], v[152:153], v[116:117]
	v_pk_add_f32 v[154:155], v[154:155], v[118:119]
	v_pk_fma_f32 v[164:165], v[116:117], v[68:69], v[164:165] op_sel:[0,1,0] op_sel_hi:[1,1,1]
	v_pk_fma_f32 v[166:167], v[118:119], v[68:69], v[166:167] op_sel:[0,1,0] op_sel_hi:[1,1,1]
	v_pk_fma_f32 v[112:113], v[70:71], v[140:141], v[144:145] op_sel:[0,0,0] op_sel_hi:[0,1,1] neg_lo:[0,0,1] neg_hi:[0,0,1]
	v_pk_fma_f32 v[114:115], v[70:71], v[142:143], v[146:147] op_sel:[0,0,0] op_sel_hi:[0,1,1] neg_lo:[0,0,1] neg_hi:[0,0,1]
	v_exp_f32_e32 v112, v112
	v_exp_f32_e32 v113, v113
	v_exp_f32_e32 v114, v114
	v_exp_f32_e32 v115, v115
	v_pk_fma_f32 v[116:117], v[70:71], v[140:141], v[144:145] op_sel:[1,0,0] op_sel_hi:[1,1,1] neg_lo:[0,0,1] neg_hi:[0,0,1]
	v_pk_fma_f32 v[118:119], v[70:71], v[142:143], v[146:147] op_sel:[1,0,0] op_sel_hi:[1,1,1] neg_lo:[0,0,1] neg_hi:[0,0,1]
	v_exp_f32_e32 v116, v116
	v_exp_f32_e32 v117, v117
	v_exp_f32_e32 v118, v118
	v_exp_f32_e32 v119, v119
	v_pk_add_f32 v[152:153], v[152:153], v[112:113]
	v_pk_add_f32 v[154:155], v[154:155], v[114:115]
	v_pk_fma_f32 v[164:165], v[112:113], v[70:71], v[164:165] op_sel:[0,0,0] op_sel_hi:[1,0,1]
	v_pk_fma_f32 v[166:167], v[114:115], v[70:71], v[166:167] op_sel:[0,0,0] op_sel_hi:[1,0,1]
	v_pk_add_f32 v[152:153], v[152:153], v[116:117]
	v_pk_add_f32 v[154:155], v[154:155], v[118:119]
	v_pk_fma_f32 v[164:165], v[116:117], v[70:71], v[164:165] op_sel:[0,1,0] op_sel_hi:[1,1,1]
	v_pk_fma_f32 v[166:167], v[118:119], v[70:71], v[166:167] op_sel:[0,1,0] op_sel_hi:[1,1,1]
	v_pk_fma_f32 v[112:113], v[92:93], v[140:141], v[144:145] op_sel:[0,0,0] op_sel_hi:[0,1,1] neg_lo:[0,0,1] neg_hi:[0,0,1]
	v_pk_fma_f32 v[114:115], v[92:93], v[142:143], v[146:147] op_sel:[0,0,0] op_sel_hi:[0,1,1] neg_lo:[0,0,1] neg_hi:[0,0,1]
	v_exp_f32_e32 v112, v112
	v_exp_f32_e32 v113, v113
	v_exp_f32_e32 v114, v114
	v_exp_f32_e32 v115, v115
	v_pk_fma_f32 v[116:117], v[92:93], v[140:141], v[144:145] op_sel:[1,0,0] op_sel_hi:[1,1,1] neg_lo:[0,0,1] neg_hi:[0,0,1]
	v_pk_fma_f32 v[118:119], v[92:93], v[142:143], v[146:147] op_sel:[1,0,0] op_sel_hi:[1,1,1] neg_lo:[0,0,1] neg_hi:[0,0,1]
	v_exp_f32_e32 v116, v116
	v_exp_f32_e32 v117, v117
	v_exp_f32_e32 v118, v118
	v_exp_f32_e32 v119, v119
	v_pk_add_f32 v[152:153], v[152:153], v[112:113]
	v_pk_add_f32 v[154:155], v[154:155], v[114:115]
	v_pk_fma_f32 v[164:165], v[112:113], v[92:93], v[164:165] op_sel:[0,0,0] op_sel_hi:[1,0,1]
	v_pk_fma_f32 v[166:167], v[114:115], v[92:93], v[166:167] op_sel:[0,0,0] op_sel_hi:[1,0,1]
	v_pk_add_f32 v[152:153], v[152:153], v[116:117]
	v_pk_add_f32 v[154:155], v[154:155], v[118:119]
	v_pk_fma_f32 v[164:165], v[116:117], v[92:93], v[164:165] op_sel:[0,1,0] op_sel_hi:[1,1,1]
	v_pk_fma_f32 v[166:167], v[118:119], v[92:93], v[166:167] op_sel:[0,1,0] op_sel_hi:[1,1,1]
	v_pk_fma_f32 v[112:113], v[94:95], v[140:141], v[144:145] op_sel:[0,0,0] op_sel_hi:[0,1,1] neg_lo:[0,0,1] neg_hi:[0,0,1]
	v_pk_fma_f32 v[114:115], v[94:95], v[142:143], v[146:147] op_sel:[0,0,0] op_sel_hi:[0,1,1] neg_lo:[0,0,1] neg_hi:[0,0,1]
	v_exp_f32_e32 v112, v112
	v_exp_f32_e32 v113, v113
	v_exp_f32_e32 v114, v114
	v_exp_f32_e32 v115, v115
	v_pk_fma_f32 v[116:117], v[94:95], v[140:141], v[144:145] op_sel:[1,0,0] op_sel_hi:[1,1,1] neg_lo:[0,0,1] neg_hi:[0,0,1]
	v_pk_fma_f32 v[118:119], v[94:95], v[142:143], v[146:147] op_sel:[1,0,0] op_sel_hi:[1,1,1] neg_lo:[0,0,1] neg_hi:[0,0,1]
	v_exp_f32_e32 v116, v116
	v_exp_f32_e32 v117, v117
	v_exp_f32_e32 v118, v118
	v_exp_f32_e32 v119, v119
	v_pk_add_f32 v[152:153], v[152:153], v[112:113]
	v_pk_add_f32 v[154:155], v[154:155], v[114:115]
	v_pk_fma_f32 v[164:165], v[112:113], v[94:95], v[164:165] op_sel:[0,0,0] op_sel_hi:[1,0,1]
	v_pk_fma_f32 v[166:167], v[114:115], v[94:95], v[166:167] op_sel:[0,0,0] op_sel_hi:[1,0,1]
	v_pk_add_f32 v[152:153], v[152:153], v[116:117]
	v_pk_add_f32 v[154:155], v[154:155], v[118:119]
	v_pk_fma_f32 v[164:165], v[116:117], v[94:95], v[164:165] op_sel:[0,1,0] op_sel_hi:[1,1,1]
	v_pk_fma_f32 v[166:167], v[118:119], v[94:95], v[166:167] op_sel:[0,1,0] op_sel_hi:[1,1,1]
	v_pk_fma_f32 v[112:113], v[100:101], v[140:141], v[144:145] op_sel:[0,0,0] op_sel_hi:[0,1,1] neg_lo:[0,0,1] neg_hi:[0,0,1]
	v_pk_fma_f32 v[114:115], v[100:101], v[142:143], v[146:147] op_sel:[0,0,0] op_sel_hi:[0,1,1] neg_lo:[0,0,1] neg_hi:[0,0,1]
	v_exp_f32_e32 v112, v112
	v_exp_f32_e32 v113, v113
	v_exp_f32_e32 v114, v114
	v_exp_f32_e32 v115, v115
	v_pk_fma_f32 v[116:117], v[100:101], v[140:141], v[144:145] op_sel:[1,0,0] op_sel_hi:[1,1,1] neg_lo:[0,0,1] neg_hi:[0,0,1]
	v_pk_fma_f32 v[118:119], v[100:101], v[142:143], v[146:147] op_sel:[1,0,0] op_sel_hi:[1,1,1] neg_lo:[0,0,1] neg_hi:[0,0,1]
	v_exp_f32_e32 v116, v116
	v_exp_f32_e32 v117, v117
	v_exp_f32_e32 v118, v118
	v_exp_f32_e32 v119, v119
	v_pk_add_f32 v[152:153], v[152:153], v[112:113]
	v_pk_add_f32 v[154:155], v[154:155], v[114:115]
	v_pk_fma_f32 v[164:165], v[112:113], v[100:101], v[164:165] op_sel:[0,0,0] op_sel_hi:[1,0,1]
	v_pk_fma_f32 v[166:167], v[114:115], v[100:101], v[166:167] op_sel:[0,0,0] op_sel_hi:[1,0,1]
	v_pk_add_f32 v[152:153], v[152:153], v[116:117]
	v_pk_add_f32 v[154:155], v[154:155], v[118:119]
	v_pk_fma_f32 v[164:165], v[116:117], v[100:101], v[164:165] op_sel:[0,1,0] op_sel_hi:[1,1,1]
	v_pk_fma_f32 v[166:167], v[118:119], v[100:101], v[166:167] op_sel:[0,1,0] op_sel_hi:[1,1,1]
	v_pk_fma_f32 v[112:113], v[102:103], v[140:141], v[144:145] op_sel:[0,0,0] op_sel_hi:[0,1,1] neg_lo:[0,0,1] neg_hi:[0,0,1]
	v_pk_fma_f32 v[114:115], v[102:103], v[142:143], v[146:147] op_sel:[0,0,0] op_sel_hi:[0,1,1] neg_lo:[0,0,1] neg_hi:[0,0,1]
	v_exp_f32_e32 v112, v112
	v_exp_f32_e32 v113, v113
	v_exp_f32_e32 v114, v114
	v_exp_f32_e32 v115, v115
	v_pk_fma_f32 v[116:117], v[102:103], v[140:141], v[144:145] op_sel:[1,0,0] op_sel_hi:[1,1,1] neg_lo:[0,0,1] neg_hi:[0,0,1]
	v_pk_fma_f32 v[118:119], v[102:103], v[142:143], v[146:147] op_sel:[1,0,0] op_sel_hi:[1,1,1] neg_lo:[0,0,1] neg_hi:[0,0,1]
	v_exp_f32_e32 v116, v116
	v_exp_f32_e32 v117, v117
	v_exp_f32_e32 v118, v118
	v_exp_f32_e32 v119, v119
	v_pk_add_f32 v[152:153], v[152:153], v[112:113]
	v_pk_add_f32 v[154:155], v[154:155], v[114:115]
	v_pk_fma_f32 v[164:165], v[112:113], v[102:103], v[164:165] op_sel:[0,0,0] op_sel_hi:[1,0,1]
	v_pk_fma_f32 v[166:167], v[114:115], v[102:103], v[166:167] op_sel:[0,0,0] op_sel_hi:[1,0,1]
	v_pk_add_f32 v[152:153], v[152:153], v[116:117]
	v_pk_add_f32 v[154:155], v[154:155], v[118:119]
	v_pk_fma_f32 v[164:165], v[116:117], v[102:103], v[164:165] op_sel:[0,1,0] op_sel_hi:[1,1,1]
	v_pk_fma_f32 v[166:167], v[118:119], v[102:103], v[166:167] op_sel:[0,1,0] op_sel_hi:[1,1,1]
	v_pk_fma_f32 v[112:113], v[104:105], v[140:141], v[144:145] op_sel:[0,0,0] op_sel_hi:[0,1,1] neg_lo:[0,0,1] neg_hi:[0,0,1]
	v_pk_fma_f32 v[114:115], v[104:105], v[142:143], v[146:147] op_sel:[0,0,0] op_sel_hi:[0,1,1] neg_lo:[0,0,1] neg_hi:[0,0,1]
	v_exp_f32_e32 v112, v112
	v_exp_f32_e32 v113, v113
	v_exp_f32_e32 v114, v114
	v_exp_f32_e32 v115, v115
	v_pk_fma_f32 v[116:117], v[104:105], v[140:141], v[144:145] op_sel:[1,0,0] op_sel_hi:[1,1,1] neg_lo:[0,0,1] neg_hi:[0,0,1]
	v_pk_fma_f32 v[118:119], v[104:105], v[142:143], v[146:147] op_sel:[1,0,0] op_sel_hi:[1,1,1] neg_lo:[0,0,1] neg_hi:[0,0,1]
	v_exp_f32_e32 v116, v116
	v_exp_f32_e32 v117, v117
	v_exp_f32_e32 v118, v118
	v_exp_f32_e32 v119, v119
	v_pk_add_f32 v[152:153], v[152:153], v[112:113]
	v_pk_add_f32 v[154:155], v[154:155], v[114:115]
	v_pk_fma_f32 v[164:165], v[112:113], v[104:105], v[164:165] op_sel:[0,0,0] op_sel_hi:[1,0,1]
	v_pk_fma_f32 v[166:167], v[114:115], v[104:105], v[166:167] op_sel:[0,0,0] op_sel_hi:[1,0,1]
	v_pk_add_f32 v[152:153], v[152:153], v[116:117]
	v_pk_add_f32 v[154:155], v[154:155], v[118:119]
	v_pk_fma_f32 v[164:165], v[116:117], v[104:105], v[164:165] op_sel:[0,1,0] op_sel_hi:[1,1,1]
	v_pk_fma_f32 v[166:167], v[118:119], v[104:105], v[166:167] op_sel:[0,1,0] op_sel_hi:[1,1,1]
	v_pk_fma_f32 v[112:113], v[106:107], v[140:141], v[144:145] op_sel:[0,0,0] op_sel_hi:[0,1,1] neg_lo:[0,0,1] neg_hi:[0,0,1]
	v_pk_fma_f32 v[114:115], v[106:107], v[142:143], v[146:147] op_sel:[0,0,0] op_sel_hi:[0,1,1] neg_lo:[0,0,1] neg_hi:[0,0,1]
	v_exp_f32_e32 v112, v112
	v_exp_f32_e32 v113, v113
	v_exp_f32_e32 v114, v114
	v_exp_f32_e32 v115, v115
	v_pk_fma_f32 v[116:117], v[106:107], v[140:141], v[144:145] op_sel:[1,0,0] op_sel_hi:[1,1,1] neg_lo:[0,0,1] neg_hi:[0,0,1]
	v_pk_fma_f32 v[118:119], v[106:107], v[142:143], v[146:147] op_sel:[1,0,0] op_sel_hi:[1,1,1] neg_lo:[0,0,1] neg_hi:[0,0,1]
	v_exp_f32_e32 v116, v116
	v_exp_f32_e32 v117, v117
	v_exp_f32_e32 v118, v118
	v_exp_f32_e32 v119, v119
	v_pk_add_f32 v[152:153], v[152:153], v[112:113]
	v_pk_add_f32 v[154:155], v[154:155], v[114:115]
	v_pk_fma_f32 v[164:165], v[112:113], v[106:107], v[164:165] op_sel:[0,0,0] op_sel_hi:[1,0,1]
	v_pk_fma_f32 v[166:167], v[114:115], v[106:107], v[166:167] op_sel:[0,0,0] op_sel_hi:[1,0,1]
	v_pk_add_f32 v[152:153], v[152:153], v[116:117]
	v_pk_add_f32 v[154:155], v[154:155], v[118:119]
	v_pk_fma_f32 v[164:165], v[116:117], v[106:107], v[164:165] op_sel:[0,1,0] op_sel_hi:[1,1,1]
	v_pk_fma_f32 v[166:167], v[118:119], v[106:107], v[166:167] op_sel:[0,1,0] op_sel_hi:[1,1,1]
	v_pk_fma_f32 v[112:113], v[108:109], v[140:141], v[144:145] op_sel:[0,0,0] op_sel_hi:[0,1,1] neg_lo:[0,0,1] neg_hi:[0,0,1]
	v_pk_fma_f32 v[114:115], v[108:109], v[142:143], v[146:147] op_sel:[0,0,0] op_sel_hi:[0,1,1] neg_lo:[0,0,1] neg_hi:[0,0,1]
	v_exp_f32_e32 v112, v112
	v_exp_f32_e32 v113, v113
	v_exp_f32_e32 v114, v114
	v_exp_f32_e32 v115, v115
	v_pk_fma_f32 v[116:117], v[108:109], v[140:141], v[144:145] op_sel:[1,0,0] op_sel_hi:[1,1,1] neg_lo:[0,0,1] neg_hi:[0,0,1]
	v_pk_fma_f32 v[118:119], v[108:109], v[142:143], v[146:147] op_sel:[1,0,0] op_sel_hi:[1,1,1] neg_lo:[0,0,1] neg_hi:[0,0,1]
	v_exp_f32_e32 v116, v116
	v_exp_f32_e32 v117, v117
	v_exp_f32_e32 v118, v118
	v_exp_f32_e32 v119, v119
	v_pk_add_f32 v[152:153], v[152:153], v[112:113]
	v_pk_add_f32 v[154:155], v[154:155], v[114:115]
	v_pk_fma_f32 v[164:165], v[112:113], v[108:109], v[164:165] op_sel:[0,0,0] op_sel_hi:[1,0,1]
	v_pk_fma_f32 v[166:167], v[114:115], v[108:109], v[166:167] op_sel:[0,0,0] op_sel_hi:[1,0,1]
	v_pk_add_f32 v[152:153], v[152:153], v[116:117]
	v_pk_add_f32 v[154:155], v[154:155], v[118:119]
	v_pk_fma_f32 v[164:165], v[116:117], v[108:109], v[164:165] op_sel:[0,1,0] op_sel_hi:[1,1,1]
	v_pk_fma_f32 v[166:167], v[118:119], v[108:109], v[166:167] op_sel:[0,1,0] op_sel_hi:[1,1,1]
	v_pk_fma_f32 v[112:113], v[110:111], v[140:141], v[144:145] op_sel:[0,0,0] op_sel_hi:[0,1,1] neg_lo:[0,0,1] neg_hi:[0,0,1]
	v_pk_fma_f32 v[114:115], v[110:111], v[142:143], v[146:147] op_sel:[0,0,0] op_sel_hi:[0,1,1] neg_lo:[0,0,1] neg_hi:[0,0,1]
	v_exp_f32_e32 v112, v112
	v_exp_f32_e32 v113, v113
	v_exp_f32_e32 v114, v114
	v_exp_f32_e32 v115, v115
	v_pk_fma_f32 v[116:117], v[110:111], v[140:141], v[144:145] op_sel:[1,0,0] op_sel_hi:[1,1,1] neg_lo:[0,0,1] neg_hi:[0,0,1]
	v_pk_fma_f32 v[118:119], v[110:111], v[142:143], v[146:147] op_sel:[1,0,0] op_sel_hi:[1,1,1] neg_lo:[0,0,1] neg_hi:[0,0,1]
	v_exp_f32_e32 v116, v116
	v_exp_f32_e32 v117, v117
	v_exp_f32_e32 v118, v118
	v_exp_f32_e32 v119, v119
	v_pk_add_f32 v[152:153], v[152:153], v[112:113]
	v_pk_add_f32 v[154:155], v[154:155], v[114:115]
	v_pk_fma_f32 v[164:165], v[112:113], v[110:111], v[164:165] op_sel:[0,0,0] op_sel_hi:[1,0,1]
	v_pk_fma_f32 v[166:167], v[114:115], v[110:111], v[166:167] op_sel:[0,0,0] op_sel_hi:[1,0,1]
	v_pk_add_f32 v[152:153], v[152:153], v[116:117]
	v_pk_add_f32 v[154:155], v[154:155], v[118:119]
	v_pk_fma_f32 v[164:165], v[116:117], v[110:111], v[164:165] op_sel:[0,1,0] op_sel_hi:[1,1,1]
	v_pk_fma_f32 v[166:167], v[118:119], v[110:111], v[166:167] op_sel:[0,1,0] op_sel_hi:[1,1,1]
	v_mov_b32_e32 v73, v164
	v_mov_b32_e32 v56, v165
	v_mov_b32_e32 v48, v166
	v_mov_b32_e32 v9, v167
	s_waitcnt lgkmcnt(0)
	s_waitcnt lgkmcnt(0)
	s_waitcnt lgkmcnt(0)
	ds_read_b128 v[128:131], v99 offset:1600
	ds_read_b128 v[182:185], v99 offset:1632
	s_waitcnt lgkmcnt(0)
	v_pk_add_f32 v[186:187], v[128:129], v[44:45]
	v_mov_b32_e32 v4, v152
	v_and_b32_e32 v0, 32, v0
	v_mov_b32_e32 v44, v4
	v_mov_b32_e32 v45, v4
	s_nop 1
	v_permlane32_swap_b32_e32 v44, v45
	v_cmp_eq_u32_e32 vcc, 0, v0
	v_mov_b32_e32 v83, v73
	v_pk_add_f32 v[188:189], v[130:131], v[46:47]
	v_cndmask_b32_e32 v0, v44, v45, vcc
	v_add_f32_e32 v0, v4, v0
	v_mov_b32_e32 v4, v73
	v_rcp_f32_e32 v0, v0
	s_nop 0
	v_permlane32_swap_b32_e32 v4, v83
	v_cndmask_b32_e32 v4, v4, v83, vcc
	v_add_f32_e32 v4, v73, v4
	v_mul_f32_e32 v0, v4, v0
	ds_read_b128 v[44:47], v99 offset:576
	ds_read_b128 v[128:131], v99 offset:608
	v_mov_b32_e32 v4, v153
	s_waitcnt lgkmcnt(0)
	v_pk_fma_f32 v[186:187], v[0:1], v[44:45], v[186:187] op_sel_hi:[0,1,1]
	v_mov_b32_e32 v8, v4
	v_mov_b32_e32 v44, v4
	s_nop 1
	v_permlane32_swap_b32_e32 v8, v44
	v_cndmask_b32_e32 v8, v8, v44, vcc
	v_add_f32_e32 v4, v4, v8
	v_mov_b32_e32 v8, v56
	v_mov_b32_e32 v67, v56
	v_rcp_f32_e32 v4, v4
	s_nop 0
	v_permlane32_swap_b32_e32 v8, v67
	v_cndmask_b32_e32 v8, v8, v67, vcc
	v_add_f32_e32 v8, v56, v8
	v_mul_f32_e32 v4, v8, v4
	v_pk_fma_f32 v[188:189], v[0:1], v[46:47], v[188:189] op_sel_hi:[0,1,1]
	ds_read_b128 v[44:47], v99 offset:832
	ds_read_b128 v[120:123], v99 offset:864
	v_mov_b32_e32 v8, v154
	s_waitcnt lgkmcnt(0)
	v_pk_fma_f32 v[84:85], v[4:5], v[44:45], v[186:187] op_sel_hi:[0,1,1]
	v_mov_b32_e32 v12, v8
	v_mov_b32_e32 v44, v8
	s_nop 1
	v_permlane32_swap_b32_e32 v12, v44
	v_cndmask_b32_e32 v12, v12, v44, vcc
	v_add_f32_e32 v8, v8, v12
	v_mov_b32_e32 v12, v48
	v_mov_b32_e32 v53, v48
	v_rcp_f32_e32 v8, v8
	s_nop 0
	v_permlane32_swap_b32_e32 v12, v53
	v_cndmask_b32_e32 v12, v12, v53, vcc
	v_add_f32_e32 v12, v48, v12
	v_mul_f32_e32 v62, v12, v8
	v_pk_fma_f32 v[90:91], v[4:5], v[46:47], v[188:189] op_sel_hi:[0,1,1]
	ds_read_b128 v[44:47], v99 offset:1088
	ds_read_b128 v[76:79], v99 offset:1120
	v_pk_add_f32 v[40:41], v[182:183], v[40:41]
	v_pk_add_f32 v[42:43], v[184:185], v[42:43]
	v_pk_fma_f32 v[40:41], v[0:1], v[128:129], v[40:41] op_sel_hi:[0,1,1]
	v_pk_fma_f32 v[42:43], v[0:1], v[130:131], v[42:43] op_sel_hi:[0,1,1]
	s_waitcnt lgkmcnt(0)
	v_pk_fma_f32 v[56:57], v[62:63], v[44:45], v[84:85] op_sel_hi:[0,1,1]
	v_pk_fma_f32 v[66:67], v[62:63], v[46:47], v[90:91] op_sel_hi:[0,1,1]
	v_pk_fma_f32 v[44:45], v[4:5], v[120:121], v[40:41] op_sel_hi:[0,1,1]
	v_pk_fma_f32 v[46:47], v[4:5], v[122:123], v[42:43] op_sel_hi:[0,1,1]
	ds_read_b128 v[40:43], v99 offset:1664
	v_pk_fma_f32 v[72:73], v[62:63], v[76:77], v[44:45] op_sel_hi:[0,1,1]
	v_pk_fma_f32 v[84:85], v[62:63], v[78:79], v[46:47] op_sel_hi:[0,1,1]
	ds_read_b128 v[44:47], v99 offset:1696
	ds_read_b128 v[76:79], v99 offset:640
	s_waitcnt lgkmcnt(0)
	v_pk_add_f32 v[80:81], v[40:41], v[36:37]
	v_pk_add_f32 v[82:83], v[42:43], v[38:39]
	ds_read_b128 v[36:39], v99 offset:672
	ds_read_b128 v[40:43], v99 offset:896
	v_pk_fma_f32 v[86:87], v[0:1], v[76:77], v[80:81] op_sel_hi:[0,1,1]
	v_pk_fma_f32 v[90:91], v[0:1], v[78:79], v[82:83] op_sel_hi:[0,1,1]
	ds_read_b128 v[76:79], v99 offset:1152
	ds_read_b128 v[80:83], v99 offset:928
	s_waitcnt lgkmcnt(0)
	v_pk_fma_f32 v[86:87], v[4:5], v[40:41], v[86:87] op_sel_hi:[0,1,1]
	v_pk_fma_f32 v[90:91], v[4:5], v[42:43], v[90:91] op_sel_hi:[0,1,1]
	ds_read_b128 v[40:43], v99 offset:1184
	v_pk_add_f32 v[32:33], v[44:45], v[32:33]
	v_pk_add_f32 v[34:35], v[46:47], v[34:35]
	v_pk_fma_f32 v[32:33], v[0:1], v[36:37], v[32:33] op_sel_hi:[0,1,1]
	v_pk_fma_f32 v[34:35], v[0:1], v[38:39], v[34:35] op_sel_hi:[0,1,1]
	v_pk_fma_f32 v[36:37], v[4:5], v[80:81], v[32:33] op_sel_hi:[0,1,1]
	v_pk_fma_f32 v[38:39], v[4:5], v[82:83], v[34:35] op_sel_hi:[0,1,1]
	ds_read_b128 v[32:35], v99 offset:1728
	s_waitcnt lgkmcnt(0)
	v_pk_fma_f32 v[80:81], v[62:63], v[40:41], v[36:37] op_sel_hi:[0,1,1]
	v_pk_fma_f32 v[82:83], v[62:63], v[42:43], v[38:39] op_sel_hi:[0,1,1]
	ds_read_b128 v[36:39], v99 offset:1760
	ds_read_b128 v[40:43], v99 offset:704
	v_mov_b32_e32 v8, v155
	v_pk_add_f32 v[44:45], v[32:33], v[28:29]
	v_pk_add_f32 v[46:47], v[34:35], v[30:31]
	ds_read_b128 v[28:31], v99 offset:736
	ds_read_b128 v[32:35], v99 offset:960
	v_mov_b32_e32 v10, v8
	v_mov_b32_e32 v11, v8
	s_nop 1
	v_permlane32_swap_b32_e32 v10, v11
	v_cndmask_b32_e32 v10, v10, v11, vcc
	v_pk_fma_f32 v[76:77], v[62:63], v[76:77], v[86:87] op_sel_hi:[0,1,1]
	v_pk_fma_f32 v[78:79], v[62:63], v[78:79], v[90:91] op_sel_hi:[0,1,1]
	s_waitcnt lgkmcnt(0)
	v_pk_fma_f32 v[86:87], v[0:1], v[40:41], v[44:45] op_sel_hi:[0,1,1]
	v_pk_fma_f32 v[90:91], v[0:1], v[42:43], v[46:47] op_sel_hi:[0,1,1]
	ds_read_b128 v[40:43], v99 offset:1216
	ds_read_b128 v[44:47], v99 offset:992
	v_add_f32_e32 v8, v8, v10
	v_mov_b32_e32 v10, v9
	v_mov_b32_e32 v11, v9
	s_nop 1
	v_permlane32_swap_b32_e32 v10, v11
	v_pk_fma_f32 v[86:87], v[4:5], v[32:33], v[86:87] op_sel_hi:[0,1,1]
	v_pk_fma_f32 v[90:91], v[4:5], v[34:35], v[90:91] op_sel_hi:[0,1,1]
	ds_read_b128 v[32:35], v99 offset:1248
	v_rcp_f32_e32 v8, v8
	v_cndmask_b32_e32 v14, v10, v11, vcc
	ds_read_b128 v[10:13], v99 offset:1344
	s_waitcnt lgkmcnt(0)
	v_pk_fma_f32 v[86:87], v[62:63], v[40:41], v[86:87] op_sel_hi:[0,1,1]
	v_pk_fma_f32 v[90:91], v[62:63], v[42:43], v[90:91] op_sel_hi:[0,1,1]
	v_add_f32_e32 v9, v9, v14
	ds_read_b128 v[14:17], v99 offset:1824
	ds_read_b128 v[40:43], v99 offset:1376
	v_mul_f32_e32 v60, v9, v8
	v_pk_fma_f32 v[68:69], v[60:61], v[10:11], v[56:57] op_sel_hi:[0,1,1]
	ds_read_b128 v[8:11], v99 offset:800
	s_waitcnt lgkmcnt(0)
	v_pk_add_f32 v[26:27], v[16:17], v[26:27]
	ds_read_b128 v[16:19], v99 offset:1056
	ds_read_b128 v[48:51], v99 offset:1792
	v_pk_fma_f32 v[66:67], v[60:61], v[12:13], v[66:67] op_sel_hi:[0,1,1]
	v_pk_add_f32 v[22:23], v[14:15], v[22:23]
	ds_read_b128 v[12:15], v99 offset:768
	v_pk_fma_f32 v[26:27], v[0:1], v[10:11], v[26:27] op_sel_hi:[0,1,1]
	v_pk_fma_f32 v[22:23], v[0:1], v[8:9], v[22:23] op_sel_hi:[0,1,1]
	ds_read_b128 v[8:11], v99 offset:1024
	ds_read_b128 v[52:55], v99 offset:1312
	s_waitcnt lgkmcnt(0)
	v_pk_fma_f32 v[26:27], v[4:5], v[18:19], v[26:27] op_sel_hi:[0,1,1]
	v_pk_fma_f32 v[22:23], v[4:5], v[16:17], v[22:23] op_sel_hi:[0,1,1]
	ds_read_b128 v[16:19], v99 offset:1280
	v_pk_add_f32 v[2:3], v[48:49], v[2:3]
	v_pk_add_f32 v[20:21], v[50:51], v[20:21]
	v_pk_fma_f32 v[2:3], v[0:1], v[12:13], v[2:3] op_sel_hi:[0,1,1]
	v_pk_fma_f32 v[2:3], v[4:5], v[8:9], v[2:3] op_sel_hi:[0,1,1]
	s_waitcnt lgkmcnt(0)
	v_pk_fma_f32 v[12:13], v[62:63], v[16:17], v[2:3] op_sel_hi:[0,1,1]
	v_pk_add_f32 v[2:3], v[36:37], v[6:7]
	v_pk_add_f32 v[6:7], v[38:39], v[24:25]
	v_pk_fma_f32 v[14:15], v[0:1], v[14:15], v[20:21] op_sel_hi:[0,1,1]
	v_pk_fma_f32 v[2:3], v[0:1], v[28:29], v[2:3] op_sel_hi:[0,1,1]
	v_pk_fma_f32 v[6:7], v[0:1], v[30:31], v[6:7] op_sel_hi:[0,1,1]
	v_add_f32_e32 v0, 0, v68
	v_add_f32_e32 v0, v69, v0
	v_pk_fma_f32 v[10:11], v[4:5], v[10:11], v[14:15] op_sel_hi:[0,1,1]
	v_pk_fma_f32 v[14:15], v[4:5], v[44:45], v[2:3] op_sel_hi:[0,1,1]
	v_pk_fma_f32 v[16:17], v[4:5], v[46:47], v[6:7] op_sel_hi:[0,1,1]
	v_add_f32_e32 v0, v66, v0
	ds_read_b128 v[56:59], v99 offset:1568
	v_pk_fma_f32 v[26:27], v[62:63], v[54:55], v[26:27] op_sel_hi:[0,1,1]
	v_pk_fma_f32 v[22:23], v[62:63], v[52:53], v[22:23] op_sel_hi:[0,1,1]
	ds_read_b128 v[52:55], v99 offset:1536
	v_lshlrev_b32_e32 v100, 2, v5
	ds_read_b128 v[2:5], v99 offset:1408
	ds_read_b128 v[6:9], v99 offset:1440
	v_pk_fma_f32 v[24:25], v[62:63], v[32:33], v[14:15] op_sel_hi:[0,1,1]
	v_pk_fma_f32 v[32:33], v[62:63], v[34:35], v[16:17] op_sel_hi:[0,1,1]
	v_pk_fma_f32 v[34:35], v[60:61], v[40:41], v[72:73] op_sel_hi:[0,1,1]
	v_add_f32_e32 v0, v67, v0
	v_add_f32_e32 v0, v34, v0
	v_pk_fma_f32 v[36:37], v[60:61], v[42:43], v[84:85] op_sel_hi:[0,1,1]
	v_add_f32_e32 v0, v35, v0
	v_add_f32_e32 v0, v36, v0
	v_add_f32_e32 v0, v37, v0
	s_waitcnt lgkmcnt(0)
	v_pk_fma_f32 v[2:3], v[60:61], v[2:3], v[76:77] op_sel_hi:[0,1,1]
	v_add_f32_e32 v0, v2, v0
	v_add_f32_e32 v0, v3, v0
	v_pk_fma_f32 v[4:5], v[60:61], v[4:5], v[78:79] op_sel_hi:[0,1,1]
	v_pk_fma_f32 v[10:11], v[62:63], v[18:19], v[10:11] op_sel_hi:[0,1,1]
	v_add_f32_e32 v0, v4, v0
	v_pk_fma_f32 v[28:29], v[60:61], v[54:55], v[10:11] op_sel_hi:[0,1,1]
	v_pk_fma_f32 v[30:31], v[60:61], v[52:53], v[12:13] op_sel_hi:[0,1,1]
	ds_read_b128 v[10:13], v99 offset:1472
	ds_read_b128 v[14:17], v99 offset:1504
	v_add_f32_e32 v0, v5, v0
	v_pk_fma_f32 v[6:7], v[60:61], v[6:7], v[80:81] op_sel_hi:[0,1,1]
	v_add_f32_e32 v0, v6, v0
	v_add_f32_e32 v0, v7, v0
	v_pk_fma_f32 v[8:9], v[60:61], v[8:9], v[82:83] op_sel_hi:[0,1,1]
	v_add_f32_e32 v0, v8, v0
	v_add_f32_e32 v0, v9, v0
	s_waitcnt lgkmcnt(0)
	v_pk_fma_f32 v[10:11], v[60:61], v[10:11], v[86:87] op_sel_hi:[0,1,1]
	v_add_f32_e32 v0, v10, v0
	v_add_f32_e32 v0, v11, v0
	v_pk_fma_f32 v[12:13], v[60:61], v[12:13], v[90:91] op_sel_hi:[0,1,1]
	v_add_f32_e32 v0, v12, v0
	v_add_f32_e32 v0, v13, v0
	v_pk_fma_f32 v[14:15], v[60:61], v[14:15], v[24:25] op_sel_hi:[0,1,1]
	v_add_f32_e32 v0, v14, v0
	v_pk_fma_f32 v[16:17], v[60:61], v[16:17], v[32:33] op_sel_hi:[0,1,1]
	v_add_f32_e32 v0, v15, v0
	v_add_f32_e32 v0, v16, v0
	v_add_f32_e32 v0, v17, v0
	v_add_f32_e32 v0, v30, v0
	v_add_f32_e32 v0, v31, v0
	v_add_f32_e32 v0, v28, v0
	v_pk_fma_f32 v[22:23], v[60:61], v[56:57], v[22:23] op_sel_hi:[0,1,1]
	v_add_f32_e32 v0, v29, v0
	v_add_f32_e32 v0, v22, v0
	v_pk_fma_f32 v[26:27], v[60:61], v[58:59], v[26:27] op_sel_hi:[0,1,1]
	v_add_f32_e32 v0, v23, v0
	v_add_f32_e32 v0, v26, v0
	v_add_f32_e32 v0, v27, v0
	v_mov_b32_e32 v24, v0
	v_mov_b32_e32 v25, v0
	s_nop 1
	v_permlane32_swap_b32_e32 v24, v25
	v_cndmask_b32_e32 v24, v24, v25, vcc
	v_add_f32_e32 v0, v0, v24
	v_mul_f32_e32 v0, 0x3c800000, v0
	v_pk_add_f32 v[24:25], v[68:69], v[0:1] op_sel_hi:[1,0] neg_lo:[0,1] neg_hi:[0,1]
	v_pk_add_f32 v[38:39], v[66:67], v[0:1] op_sel_hi:[1,0] neg_lo:[0,1] neg_hi:[0,1]
	v_pk_mul_f32 v[32:33], v[24:25], v[24:25]
	v_pk_mul_f32 v[40:41], v[38:39], v[38:39]
	v_pk_add_f32 v[34:35], v[34:35], v[0:1] op_sel_hi:[1,0] neg_lo:[0,1] neg_hi:[0,1]
	v_pk_add_f32 v[36:37], v[36:37], v[0:1] op_sel_hi:[1,0] neg_lo:[0,1] neg_hi:[0,1]
	v_pk_add_f32 v[46:47], v[2:3], v[0:1] op_sel_hi:[1,0] neg_lo:[0,1] neg_hi:[0,1]
	v_pk_add_f32 v[48:49], v[4:5], v[0:1] op_sel_hi:[1,0] neg_lo:[0,1] neg_hi:[0,1]
	v_pk_add_f32 v[50:51], v[6:7], v[0:1] op_sel_hi:[1,0] neg_lo:[0,1] neg_hi:[0,1]
	v_pk_add_f32 v[52:53], v[8:9], v[0:1] op_sel_hi:[1,0] neg_lo:[0,1] neg_hi:[0,1]
	v_pk_add_f32 v[54:55], v[10:11], v[0:1] op_sel_hi:[1,0] neg_lo:[0,1] neg_hi:[0,1]
	v_pk_add_f32 v[56:57], v[12:13], v[0:1] op_sel_hi:[1,0] neg_lo:[0,1] neg_hi:[0,1]
	v_pk_add_f32 v[58:59], v[14:15], v[0:1] op_sel_hi:[1,0] neg_lo:[0,1] neg_hi:[0,1]
	v_pk_add_f32 v[60:61], v[16:17], v[0:1] op_sel_hi:[1,0] neg_lo:[0,1] neg_hi:[0,1]
	v_pk_add_f32 v[30:31], v[30:31], v[0:1] op_sel_hi:[1,0] neg_lo:[0,1] neg_hi:[0,1]
	v_pk_add_f32 v[28:29], v[28:29], v[0:1] op_sel_hi:[1,0] neg_lo:[0,1] neg_hi:[0,1]
	v_pk_add_f32 v[22:23], v[22:23], v[0:1] op_sel_hi:[1,0] neg_lo:[0,1] neg_hi:[0,1]
	v_pk_add_f32 v[26:27], v[26:27], v[0:1] op_sel_hi:[1,0] neg_lo:[0,1] neg_hi:[0,1]
	v_add_f32_e32 v0, v32, v33
	v_add_f32_e32 v0, v40, v0
	v_pk_mul_f32 v[42:43], v[34:35], v[34:35]
	v_add_f32_e32 v0, v41, v0
	v_add_f32_e32 v0, v42, v0
	v_pk_mul_f32 v[44:45], v[36:37], v[36:37]
	v_add_f32_e32 v0, v43, v0
	v_add_f32_e32 v0, v44, v0
	v_pk_mul_f32 v[2:3], v[46:47], v[46:47]
	v_add_f32_e32 v0, v45, v0
	v_add_f32_e32 v0, v2, v0
	v_pk_mul_f32 v[4:5], v[48:49], v[48:49]
	v_add_f32_e32 v0, v3, v0
	v_add_f32_e32 v0, v4, v0
	v_pk_mul_f32 v[6:7], v[50:51], v[50:51]
	v_add_f32_e32 v0, v5, v0
	v_add_f32_e32 v0, v6, v0
	v_pk_mul_f32 v[8:9], v[52:53], v[52:53]
	v_add_f32_e32 v0, v7, v0
	v_add_f32_e32 v0, v8, v0
	v_pk_mul_f32 v[10:11], v[54:55], v[54:55]
	v_add_f32_e32 v0, v9, v0
	v_add_f32_e32 v0, v10, v0
	v_pk_mul_f32 v[12:13], v[56:57], v[56:57]
	v_add_f32_e32 v0, v11, v0
	v_add_f32_e32 v0, v12, v0
	v_pk_mul_f32 v[14:15], v[58:59], v[58:59]
	v_add_f32_e32 v0, v13, v0
	v_add_f32_e32 v0, v14, v0
	v_pk_mul_f32 v[16:17], v[60:61], v[60:61]
	v_add_f32_e32 v0, v15, v0
	v_add_f32_e32 v0, v16, v0
	v_pk_mul_f32 v[32:33], v[30:31], v[30:31]
	v_add_f32_e32 v0, v17, v0
	v_add_f32_e32 v0, v32, v0
	v_pk_mul_f32 v[2:3], v[28:29], v[28:29]
	v_add_f32_e32 v0, v33, v0
	v_add_f32_e32 v0, v2, v0
	v_pk_mul_f32 v[4:5], v[22:23], v[22:23]
	v_add_f32_e32 v0, v3, v0
	v_add_f32_e32 v0, v4, v0
	v_pk_mul_f32 v[6:7], v[26:27], v[26:27]
	v_add_f32_e32 v0, v5, v0
	v_add_f32_e32 v0, v6, v0
	v_add_f32_e32 v0, v7, v0
	v_mov_b32_e32 v2, v0
	v_mov_b32_e32 v3, v0
	s_nop 1
	v_permlane32_swap_b32_e32 v2, v3
	v_cndmask_b32_e32 v2, v2, v3, vcc
	v_add_f32_e32 v0, v0, v2
	v_mov_b32_e32 v2, 0x3727c5ac
	v_fmac_f32_e32 v2, 0x3c800000, v0
	ds_read_b128 v[18:21], v99 offset:3392
	v_rsq_f32_e32 v0, v2
	ds_read_b128 v[2:5], v99 offset:3136
	ds_read_b128 v[6:9], v99 offset:3168
	ds_read_b128 v[10:13], v99 offset:3424
	ds_read_b128 v[14:17], v99 offset:3456
	s_load_dwordx2 s[0:1], s[0:1], 0x40
	v_lshlrev_b32_e32 v101, 4, v1
	v_pk_mul_f32 v[24:25], v[24:25], v[0:1] op_sel_hi:[1,0]
	s_mov_b32 s2, 8
	s_waitcnt lgkmcnt(0)
	v_pk_fma_f32 v[86:87], v[2:3], v[24:25], v[18:19]
	v_pk_mul_f32 v[2:3], v[38:39], v[0:1] op_sel_hi:[1,0]
	v_pk_mul_f32 v[24:25], v[34:35], v[0:1] op_sel_hi:[1,0]
	v_pk_fma_f32 v[84:85], v[4:5], v[2:3], v[20:21]
	ds_read_b128 v[2:5], v99 offset:3200
	ds_read_b128 v[18:21], v99 offset:3232
	v_pk_fma_f32 v[82:83], v[6:7], v[24:25], v[10:11]
	v_pk_mul_f32 v[6:7], v[36:37], v[0:1] op_sel_hi:[1,0]
	v_pk_mul_f32 v[24:25], v[46:47], v[0:1] op_sel_hi:[1,0]
	v_pk_fma_f32 v[80:81], v[8:9], v[6:7], v[12:13]
	ds_read_b128 v[6:9], v99 offset:3488
	ds_read_b128 v[10:13], v99 offset:3520
	s_waitcnt lgkmcnt(0)
	v_pk_fma_f32 v[78:79], v[2:3], v[24:25], v[14:15]
	v_pk_mul_f32 v[2:3], v[48:49], v[0:1] op_sel_hi:[1,0]
	v_pk_mul_f32 v[24:25], v[50:51], v[0:1] op_sel_hi:[1,0]
	v_pk_fma_f32 v[76:77], v[4:5], v[2:3], v[16:17]
	ds_read_b128 v[2:5], v99 offset:3264
	ds_read_b128 v[14:17], v99 offset:3296
	v_pk_fma_f32 v[74:75], v[18:19], v[24:25], v[6:7]
	v_pk_mul_f32 v[6:7], v[52:53], v[0:1] op_sel_hi:[1,0]
	v_pk_mul_f32 v[24:25], v[54:55], v[0:1] op_sel_hi:[1,0]
	v_pk_fma_f32 v[72:73], v[20:21], v[6:7], v[8:9]
	ds_read_b128 v[6:9], v99 offset:3552
	ds_read_b128 v[18:21], v99 offset:3584
	s_waitcnt lgkmcnt(0)
	v_pk_fma_f32 v[70:71], v[2:3], v[24:25], v[10:11]
	v_pk_mul_f32 v[2:3], v[56:57], v[0:1] op_sel_hi:[1,0]
	v_pk_mul_f32 v[24:25], v[58:59], v[0:1] op_sel_hi:[1,0]
	v_pk_fma_f32 v[68:69], v[4:5], v[2:3], v[12:13]
	ds_read_b128 v[2:5], v99 offset:3328
	ds_read_b128 v[10:13], v99 offset:3360
	v_pk_fma_f32 v[66:67], v[14:15], v[24:25], v[6:7]
	v_pk_mul_f32 v[6:7], v[60:61], v[0:1] op_sel_hi:[1,0]
	v_pk_mul_f32 v[14:15], v[30:31], v[0:1] op_sel_hi:[1,0]
	v_pk_fma_f32 v[96:97], v[16:17], v[6:7], v[8:9]
	ds_read_b128 v[6:9], v99 offset:3616
	s_waitcnt lgkmcnt(0)
	v_pk_fma_f32 v[88:89], v[2:3], v[14:15], v[18:19]
	v_pk_mul_f32 v[2:3], v[28:29], v[0:1] op_sel_hi:[1,0]
	s_waitcnt vmcnt(0)
	v_cvt_pkrtz_f16_f32 v48, v86, v87
	v_pk_fma_f32 v[90:91], v[4:5], v[2:3], v[20:21]
	v_pk_mul_f32 v[2:3], v[22:23], v[0:1] op_sel_hi:[1,0]
	v_cvt_pkrtz_f16_f32 v49, v84, v85
	v_pk_fma_f32 v[92:93], v[10:11], v[2:3], v[6:7]
	v_pk_mul_f32 v[2:3], v[26:27], v[0:1] op_sel_hi:[1,0]
	v_mov_b32_e32 v0, 0
	v_pk_fma_f32 v[94:95], v[12:13], v[2:3], v[8:9]
	v_cvt_pkrtz_f16_f32 v50, v82, v83
	v_cvt_pkrtz_f16_f32 v51, v80, v81
	v_cvt_pkrtz_f16_f32 v52, v78, v79
	v_cvt_pkrtz_f16_f32 v53, v76, v77
	v_cvt_pkrtz_f16_f32 v54, v74, v75
	v_cvt_pkrtz_f16_f32 v55, v72, v73
	v_cvt_pkrtz_f16_f32 v56, v70, v71
	v_cvt_pkrtz_f16_f32 v57, v68, v69
	v_cvt_pkrtz_f16_f32 v58, v66, v67
	v_cvt_pkrtz_f16_f32 v59, v96, v97
	v_cvt_pkrtz_f16_f32 v60, v88, v89
	v_cvt_pkrtz_f16_f32 v61, v90, v91
	v_cvt_pkrtz_f16_f32 v62, v92, v93
	v_cvt_pkrtz_f16_f32 v63, v94, v95
	v_or_b32_e32 v102, 0x8000, v101
	s_waitcnt vmcnt(0)
	s_barrier
	v_add_u32_e32 v156, 0x10740, v98
	ds_read_b128 v[16:19], v99 offset:2880
	ds_read_b128 v[20:23], v99 offset:2912
	ds_read_b128 v[24:27], v99 offset:2944
	ds_read_b128 v[28:31], v99 offset:2976
	ds_read_b128 v[0:3], v99 offset:3008
	ds_read_b128 v[4:7], v99 offset:3040
	ds_read_b128 v[8:11], v99 offset:3072
	ds_read_b128 v[12:15], v99 offset:3104
	s_mov_b32 s2, 8
.Lmy_ffn3_k1:
	ds_read_b128 v[32:35], v156
	ds_read_b128 v[36:39], v156 offset:32
	ds_read_b128 v[40:43], v156 offset:64
	ds_read_b128 v[44:47], v156 offset:96
	ds_read_b128 v[140:143], v101
	ds_read_b128 v[144:147], v101 offset:1024
	ds_read_b128 v[148:151], v101 offset:2048
	ds_read_b128 v[152:155], v101 offset:3072
	v_add_u32_e32 v101, 0x1000, v101
	v_add_u32_e32 v156, 0x80, v156
	s_add_i32 s2, s2, -1
	s_waitcnt lgkmcnt(3)
	v_mfma_f32_32x32x16_f16 v[32:47], v[140:143], v[48:51], v[32:47]
	s_waitcnt lgkmcnt(2)
	v_mfma_f32_32x32x16_f16 v[32:47], v[144:147], v[52:55], v[32:47]
	s_waitcnt lgkmcnt(1)
	v_mfma_f32_32x32x16_f16 v[32:47], v[148:151], v[56:59], v[32:47]
	s_waitcnt lgkmcnt(0)
	v_mfma_f32_32x32x16_f16 v[32:47], v[152:155], v[60:63], v[32:47]
	ds_read_b128 v[112:115], v102
	ds_read_b128 v[116:119], v102 offset:16384
	ds_read_b128 v[104:107], v102 offset:1024
	ds_read_b128 v[120:123], v102 offset:17408
	v_add_u32_e32 v102, 0x800, v102
	s_cmp_lg_u32 s2, 0
	s_nop 5
	v_max_f32_e32 v32, 0, v32
	v_max_f32_e32 v33, 0, v33
	v_max_f32_e32 v34, 0, v34
	v_max_f32_e32 v35, 0, v35
	v_max_f32_e32 v36, 0, v36
	v_max_f32_e32 v37, 0, v37
	v_max_f32_e32 v38, 0, v38
	v_max_f32_e32 v39, 0, v39
	v_cvt_pkrtz_f16_f32 v32, v32, v33
	v_cvt_pkrtz_f16_f32 v33, v34, v35
	v_cvt_pkrtz_f16_f32 v34, v36, v37
	v_cvt_pkrtz_f16_f32 v35, v38, v39
	s_waitcnt lgkmcnt(2)
	s_nop 0
	v_mfma_f32_32x32x16_f16 v[16:31], v[112:115], v[32:35], v[16:31]
	v_mfma_f32_32x32x16_f16 v[0:15], v[116:119], v[32:35], v[0:15]
	v_max_f32_e32 v40, 0, v40
	v_max_f32_e32 v41, 0, v41
	v_max_f32_e32 v42, 0, v42
	v_max_f32_e32 v43, 0, v43
	v_max_f32_e32 v44, 0, v44
	v_max_f32_e32 v45, 0, v45
	v_max_f32_e32 v46, 0, v46
	v_max_f32_e32 v47, 0, v47
	v_cvt_pkrtz_f16_f32 v32, v40, v41
	v_cvt_pkrtz_f16_f32 v33, v42, v43
	v_cvt_pkrtz_f16_f32 v34, v44, v45
	v_cvt_pkrtz_f16_f32 v35, v46, v47
	s_waitcnt lgkmcnt(0)
	s_nop 0
	v_mfma_f32_32x32x16_f16 v[16:31], v[104:107], v[32:35], v[16:31]
	v_mfma_f32_32x32x16_f16 v[0:15], v[120:123], v[32:35], v[0:15]
	s_cbranch_scc1 .Lmy_ffn3_k1
	s_waitcnt lgkmcnt(7)
	s_nop 0
	s_nop 7
	v_pk_add_f32 v[16:17], v[86:87], v[16:17]
	v_pk_add_f32 v[18:19], v[84:85], v[18:19]
	v_add_f32_e32 v48, 0, v16
	v_add_f32_e32 v48, v17, v48
	v_add_f32_e32 v48, v18, v48
	s_waitcnt lgkmcnt(6)
	v_add_f32_e32 v48, v19, v48
	v_pk_add_f32 v[20:21], v[82:83], v[20:21]
	v_add_f32_e32 v48, v20, v48
	v_add_f32_e32 v48, v21, v48
	v_pk_add_f32 v[22:23], v[80:81], v[22:23]
	s_waitcnt lgkmcnt(3)
	v_add_f32_e32 v48, v22, v48
	v_add_f32_e32 v48, v23, v48
	v_pk_add_f32 v[24:25], v[78:79], v[24:25]
	v_add_f32_e32 v48, v24, v48
	v_add_f32_e32 v48, v25, v48
	v_pk_add_f32 v[26:27], v[76:77], v[26:27]
	s_waitcnt lgkmcnt(2)
	v_add_f32_e32 v48, v26, v48
	v_add_f32_e32 v48, v27, v48
	v_pk_add_f32 v[28:29], v[74:75], v[28:29]
	v_add_f32_e32 v48, v28, v48
	v_add_f32_e32 v48, v29, v48
	v_pk_add_f32 v[30:31], v[72:73], v[30:31]
	v_add_f32_e32 v48, v30, v48
	v_add_f32_e32 v48, v31, v48
	v_pk_add_f32 v[0:1], v[70:71], v[0:1]
	v_add_f32_e32 v48, v0, v48
	v_add_f32_e32 v48, v1, v48
	v_pk_add_f32 v[2:3], v[68:69], v[2:3]
	v_add_f32_e32 v48, v2, v48
	v_add_f32_e32 v48, v3, v48
	v_pk_add_f32 v[4:5], v[66:67], v[4:5]
	v_add_f32_e32 v48, v4, v48
	v_pk_add_f32 v[6:7], v[96:97], v[6:7]
	v_add_f32_e32 v48, v5, v48
	s_waitcnt lgkmcnt(1)
	v_add_f32_e32 v48, v6, v48
	v_pk_add_f32 v[8:9], v[88:89], v[8:9]
	v_add_f32_e32 v48, v7, v48
	v_add_f32_e32 v48, v8, v48
	v_pk_add_f32 v[10:11], v[90:91], v[10:11]
	v_add_f32_e32 v48, v9, v48
	s_waitcnt lgkmcnt(0)
	v_add_f32_e32 v48, v10, v48
	v_pk_add_f32 v[12:13], v[92:93], v[12:13]
	v_add_f32_e32 v48, v11, v48
	v_add_f32_e32 v48, v12, v48
	v_pk_add_f32 v[14:15], v[94:95], v[14:15]
	v_add_f32_e32 v48, v13, v48
	v_add_f32_e32 v48, v14, v48
	v_add_f32_e32 v48, v15, v48
	v_mov_b32_e32 v49, v48
	v_mov_b32_e32 v50, v48
	s_nop 1
	v_permlane32_swap_b32_e32 v49, v50
	v_cndmask_b32_e32 v49, v49, v50, vcc
	v_add_f32_e32 v48, v48, v49
	v_mul_f32_e32 v48, 0x3c800000, v48
	v_pk_add_f32 v[16:17], v[16:17], v[48:49] op_sel_hi:[1,0] neg_lo:[0,1] neg_hi:[0,1]
	v_pk_add_f32 v[18:19], v[18:19], v[48:49] op_sel_hi:[1,0] neg_lo:[0,1] neg_hi:[0,1]
	v_pk_mul_f32 v[50:51], v[16:17], v[16:17]
	v_pk_mul_f32 v[52:53], v[18:19], v[18:19]
	v_add_f32_e32 v50, v50, v51
	v_pk_add_f32 v[20:21], v[20:21], v[48:49] op_sel_hi:[1,0] neg_lo:[0,1] neg_hi:[0,1]
	v_add_f32_e32 v50, v52, v50
	v_pk_mul_f32 v[54:55], v[20:21], v[20:21]
	v_add_f32_e32 v50, v53, v50
	v_pk_add_f32 v[22:23], v[22:23], v[48:49] op_sel_hi:[1,0] neg_lo:[0,1] neg_hi:[0,1]
	v_add_f32_e32 v50, v54, v50
	v_pk_mul_f32 v[56:57], v[22:23], v[22:23]
	v_add_f32_e32 v50, v55, v50
	v_pk_add_f32 v[24:25], v[24:25], v[48:49] op_sel_hi:[1,0] neg_lo:[0,1] neg_hi:[0,1]
	v_add_f32_e32 v50, v56, v50
	v_pk_mul_f32 v[58:59], v[24:25], v[24:25]
	v_add_f32_e32 v50, v57, v50
	v_pk_add_f32 v[26:27], v[26:27], v[48:49] op_sel_hi:[1,0] neg_lo:[0,1] neg_hi:[0,1]
	v_add_f32_e32 v50, v58, v50
	v_pk_mul_f32 v[60:61], v[26:27], v[26:27]
	v_add_f32_e32 v50, v59, v50
	v_pk_add_f32 v[28:29], v[28:29], v[48:49] op_sel_hi:[1,0] neg_lo:[0,1] neg_hi:[0,1]
	v_add_f32_e32 v50, v60, v50
	v_lshlrev_b64 v[62:63], 7, v[64:65]
	v_pk_mul_f32 v[64:65], v[28:29], v[28:29]
	v_add_f32_e32 v50, v61, v50
	v_pk_add_f32 v[30:31], v[30:31], v[48:49] op_sel_hi:[1,0] neg_lo:[0,1] neg_hi:[0,1]
	v_add_f32_e32 v50, v64, v50
	v_pk_mul_f32 v[66:67], v[30:31], v[30:31]
	v_add_f32_e32 v50, v65, v50
	v_pk_add_f32 v[0:1], v[0:1], v[48:49] op_sel_hi:[1,0] neg_lo:[0,1] neg_hi:[0,1]
	v_add_f32_e32 v50, v66, v50
	v_pk_mul_f32 v[68:69], v[0:1], v[0:1]
	v_add_f32_e32 v50, v67, v50
	v_pk_add_f32 v[2:3], v[2:3], v[48:49] op_sel_hi:[1,0] neg_lo:[0,1] neg_hi:[0,1]
	v_add_f32_e32 v50, v68, v50
	v_pk_mul_f32 v[70:71], v[2:3], v[2:3]
	v_add_f32_e32 v50, v69, v50
	v_pk_add_f32 v[4:5], v[4:5], v[48:49] op_sel_hi:[1,0] neg_lo:[0,1] neg_hi:[0,1]
	v_add_f32_e32 v50, v70, v50
	v_pk_mul_f32 v[72:73], v[4:5], v[4:5]
	v_add_f32_e32 v50, v71, v50
	v_pk_add_f32 v[6:7], v[6:7], v[48:49] op_sel_hi:[1,0] neg_lo:[0,1] neg_hi:[0,1]
	v_add_f32_e32 v50, v72, v50
	v_pk_add_f32 v[8:9], v[8:9], v[48:49] op_sel_hi:[1,0] neg_lo:[0,1] neg_hi:[0,1]
	v_pk_add_f32 v[10:11], v[10:11], v[48:49] op_sel_hi:[1,0] neg_lo:[0,1] neg_hi:[0,1]
	v_pk_add_f32 v[12:13], v[12:13], v[48:49] op_sel_hi:[1,0] neg_lo:[0,1] neg_hi:[0,1]
	v_pk_add_f32 v[14:15], v[14:15], v[48:49] op_sel_hi:[1,0] neg_lo:[0,1] neg_hi:[0,1]
	v_pk_mul_f32 v[48:49], v[6:7], v[6:7]
	v_add_f32_e32 v50, v73, v50
	v_add_f32_e32 v48, v48, v50
	v_pk_mul_f32 v[74:75], v[8:9], v[8:9]
	v_add_f32_e32 v48, v49, v48
	v_add_f32_e32 v48, v74, v48
	v_pk_mul_f32 v[76:77], v[10:11], v[10:11]
	v_add_f32_e32 v48, v75, v48
	v_add_f32_e32 v48, v76, v48
	v_pk_mul_f32 v[78:79], v[12:13], v[12:13]
	v_add_f32_e32 v48, v77, v48
	v_add_f32_e32 v48, v78, v48
	v_pk_mul_f32 v[80:81], v[14:15], v[14:15]
	v_add_f32_e32 v48, v79, v48
	v_add_f32_e32 v48, v80, v48
	v_add_f32_e32 v48, v81, v48
	v_mov_b32_e32 v49, v48
	v_mov_b32_e32 v50, v48
	s_nop 1
	v_permlane32_swap_b32_e32 v49, v50
	v_cndmask_b32_e32 v49, v49, v50, vcc
	v_add_f32_e32 v48, v48, v49
	v_mov_b32_e32 v49, 0x3727c5ac
	v_fmac_f32_e32 v49, 0x3c800000, v48
	v_rsq_f32_e32 v48, v49
	ds_read_b128 v[118:121], v99 offset:3648
	ds_read_b128 v[122:125], v99 offset:3680
	ds_read_b128 v[126:129], v99 offset:3904
	ds_read_b128 v[130:133], v99 offset:3936
	ds_read_b128 v[134:137], v99 offset:3712
	ds_read_b128 v[138:141], v99 offset:3744
	ds_read_b128 v[142:145], v99 offset:3968
	ds_read_b128 v[146:149], v99 offset:4000
	ds_read_b128 v[150:153], v99 offset:3776
	ds_read_b128 v[154:157], v99 offset:3808
	ds_read_b128 v[158:161], v99 offset:4032
	ds_read_b128 v[162:165], v99 offset:4064
	ds_read_b128 v[40:43], v99 offset:3840
	ds_read_b128 v[32:35], v99 offset:3872
	ds_read_b128 v[44:47], v99 offset:4096
	ds_read_b128 v[36:39], v99 offset:4128
	v_lshl_add_u64 v[62:63], s[0:1], 0, v[62:63]
	v_lshlrev_b32_e32 v50, 1, v100
	v_pk_mul_f32 v[0:1], v[0:1], v[48:49] op_sel_hi:[1,0]
	v_pk_mul_f32 v[2:3], v[2:3], v[48:49] op_sel_hi:[1,0]
	v_mov_b32_e32 v51, 0
	s_waitcnt lgkmcnt(5)
	v_pk_fma_f32 v[0:1], v[150:151], v[0:1], v[158:159]
	v_pk_fma_f32 v[2:3], v[152:153], v[2:3], v[160:161]
	v_pk_mul_f32 v[4:5], v[4:5], v[48:49] op_sel_hi:[1,0]
	v_pk_mul_f32 v[6:7], v[6:7], v[48:49] op_sel_hi:[1,0]
	v_lshl_add_u64 v[50:51], v[62:63], 0, v[50:51]
	s_waitcnt lgkmcnt(4)
	v_pk_fma_f32 v[4:5], v[154:155], v[4:5], v[162:163]
	v_pk_fma_f32 v[6:7], v[156:157], v[6:7], v[164:165]
	v_cvt_pk_f16_f32 v0, v0, v1
	v_cvt_pk_f16_f32 v1, v2, v3
	global_store_dwordx2 v[50:51], v[0:1], off offset:64
	v_cvt_pk_f16_f32 v0, v4, v5
	v_cvt_pk_f16_f32 v1, v6, v7
	v_pk_mul_f32 v[16:17], v[16:17], v[48:49] op_sel_hi:[1,0]
	v_pk_mul_f32 v[18:19], v[18:19], v[48:49] op_sel_hi:[1,0]
	global_store_dwordx2 v[50:51], v[0:1], off offset:80
	v_pk_mul_f32 v[0:1], v[8:9], v[48:49] op_sel_hi:[1,0]
	v_pk_mul_f32 v[2:3], v[10:11], v[48:49] op_sel_hi:[1,0]
	v_pk_fma_f32 v[16:17], v[118:119], v[16:17], v[126:127]
	v_pk_fma_f32 v[18:19], v[120:121], v[18:19], v[128:129]
	v_pk_mul_f32 v[20:21], v[20:21], v[48:49] op_sel_hi:[1,0]
	v_pk_mul_f32 v[22:23], v[22:23], v[48:49] op_sel_hi:[1,0]
	s_waitcnt lgkmcnt(1)
	v_pk_fma_f32 v[0:1], v[40:41], v[0:1], v[44:45]
	v_pk_fma_f32 v[2:3], v[42:43], v[2:3], v[46:47]
	v_pk_fma_f32 v[20:21], v[122:123], v[20:21], v[130:131]
	v_pk_fma_f32 v[22:23], v[124:125], v[22:23], v[132:133]
	v_pk_mul_f32 v[24:25], v[24:25], v[48:49] op_sel_hi:[1,0]
	v_pk_mul_f32 v[26:27], v[26:27], v[48:49] op_sel_hi:[1,0]
	v_cvt_pk_f16_f32 v16, v16, v17
	v_cvt_pk_f16_f32 v17, v18, v19
	v_cvt_pk_f16_f32 v0, v0, v1
	v_cvt_pk_f16_f32 v1, v2, v3
	v_pk_fma_f32 v[24:25], v[134:135], v[24:25], v[142:143]
	v_pk_fma_f32 v[26:27], v[136:137], v[26:27], v[144:145]
	v_pk_mul_f32 v[28:29], v[28:29], v[48:49] op_sel_hi:[1,0]
	v_pk_mul_f32 v[30:31], v[30:31], v[48:49] op_sel_hi:[1,0]
	global_store_dwordx2 v[50:51], v[16:17], off
	v_cvt_pk_f16_f32 v16, v20, v21
	v_cvt_pk_f16_f32 v17, v22, v23
	global_store_dwordx2 v[50:51], v[0:1], off offset:96
	v_pk_mul_f32 v[0:1], v[12:13], v[48:49] op_sel_hi:[1,0]
	v_pk_mul_f32 v[2:3], v[14:15], v[48:49] op_sel_hi:[1,0]
	v_pk_fma_f32 v[28:29], v[138:139], v[28:29], v[146:147]
	v_pk_fma_f32 v[30:31], v[140:141], v[30:31], v[148:149]
	global_store_dwordx2 v[50:51], v[16:17], off offset:16
	v_cvt_pk_f16_f32 v16, v24, v25
	v_cvt_pk_f16_f32 v17, v26, v27
	s_waitcnt lgkmcnt(0)
	v_pk_fma_f32 v[0:1], v[32:33], v[0:1], v[36:37]
	v_pk_fma_f32 v[2:3], v[34:35], v[2:3], v[38:39]
	global_store_dwordx2 v[50:51], v[16:17], off offset:32
	v_cvt_pk_f16_f32 v16, v28, v29
	v_cvt_pk_f16_f32 v17, v30, v31
	v_cvt_pk_f16_f32 v0, v0, v1
	v_cvt_pk_f16_f32 v1, v2, v3
	global_store_dwordx2 v[50:51], v[16:17], off offset:48
	global_store_dwordx2 v[50:51], v[0:1], off offset:112
	s_endpgm
